# chunk_unit pool: pool_scale loads hoisted above the window sums; c-tile loads of all four channel groups preloaded in one burst (registers -> LDS per group) instead of serial load-wait loops; one more
# baseline (speedup 1.0000x reference)
.LBB0_368:
	s_lshr_b32 s2, s21, 25
	s_add_i32 s2, s20, s2
	s_and_b32 s2, s2, 0x1ffff80
	s_sub_i32 s2, s20, s2
	s_lshl_b64 s[0:1], s[20:21], 7
	s_lshl_b32 s20, s2, 7
	s_movk_i32 s2, 0x478
	s_not_b32 s33, s20
	v_cmp_gt_i32_e64 s[4:5], s2, v52
	v_lshlrev_b32_e32 v57, 3, v52
	v_mov_b32_e32 v118, 0
	v_mov_b32_e32 v119, 0
	v_mov_b32_e32 v120, 0
	v_mov_b32_e32 v121, 0
	v_mov_b32_e32 v122, 0
	v_mov_b32_e32 v123, 0
	v_mov_b32_e32 v124, 0
	v_mov_b32_e32 v125, 0
	v_mov_b32_e32 v126, 0
	v_mov_b32_e32 v127, 0
	v_mov_b32_e32 v128, 0
	v_mov_b32_e32 v129, 0
	v_mov_b32_e32 v130, 0
	v_mov_b32_e32 v131, 0
	v_mov_b32_e32 v132, 0
	v_mov_b32_e32 v133, 0
	v_mov_b32_e32 v134, 0
	v_mov_b32_e32 v135, 0
	v_mov_b32_e32 v136, 0
	v_mov_b32_e32 v137, 0
	v_mov_b32_e32 v138, 0
	v_mov_b32_e32 v139, 0
	v_mov_b32_e32 v140, 0
	v_mov_b32_e32 v141, 0
	v_mov_b32_e32 v142, 0
	v_mov_b32_e32 v143, 0
	v_mov_b32_e32 v144, 0
	v_mov_b32_e32 v145, 0
	v_mov_b32_e32 v146, 0
	v_mov_b32_e32 v147, 0
	v_mov_b32_e32 v148, 0
	v_mov_b32_e32 v149, 0
	v_mov_b32_e32 v150, 0
	v_mov_b32_e32 v151, 0
	v_mov_b32_e32 v152, 0
	v_mov_b32_e32 v153, 0
	v_mov_b32_e32 v154, 0
	v_mov_b32_e32 v155, 0
	v_mov_b32_e32 v156, 0
	v_mov_b32_e32 v157, 0
	v_mov_b32_e32 v158, 0
	v_mov_b32_e32 v159, 0
	v_mov_b32_e32 v160, 0
	v_mov_b32_e32 v161, 0
	v_mov_b32_e32 v162, 0
	v_mov_b32_e32 v163, 0
	v_mov_b32_e32 v164, 0
	v_mov_b32_e32 v165, 0
	v_ashrrev_i32_e32 v206, 3, v52
	v_add_u32_e32 v166, -15, v206
	v_ashrrev_i32_e32 v167, 31, v166
	v_lshl_add_u64 v[168:169], s[0:1], 0, v[166:167]
	v_mov_b64_e32 v[170:171], s[10:11]
	s_movk_i32 s98, 0x1200
	v_mad_u64_u32 v[170:171], s[100:101], v168, s98, v[170:171]
	v_mad_i32_i24 v171, v169, s98, v171
	v_and_b32_e32 v172, 7, v52
	v_lshlrev_b32_e32 v172, 4, v172
	v_mov_b32_e32 v173, 0
	v_lshl_add_u64 v[170:171], v[170:171], 0, v[172:173]
	v_add_co_u32_e32 v170, vcc, 0x1000, v170
	s_nop 1
	v_addc_co_u32_e32 v171, vcc, 0, v171, vcc
	s_mov_b64 s[100:101], 0x48000
	v_lshl_add_u64 v[174:175], v[170:171], 0, s[100:101]
	v_lshl_add_u64 v[176:177], v[174:175], 0, s[100:101]
	v_lshlrev_b32_e32 v204, 5, v52
	s_mov_b64 s[98:99], exec
	v_cmp_lt_i32_e32 vcc, s33, v166
	s_and_b64 exec, s[98:99], vcc
	global_load_dwordx4 v[118:121], v[170:171], off
	global_load_dwordx4 v[130:133], v[170:171], off offset:128
	global_load_dwordx4 v[142:145], v[170:171], off offset:256
	global_load_dwordx4 v[154:157], v[170:171], off offset:384
	s_mov_b64 exec, s[98:99]
	v_add_u32_e32 v178, 64, v166
	v_cmp_lt_i32_e32 vcc, s33, v178
	s_and_b64 exec, s[98:99], vcc
	global_load_dwordx4 v[122:125], v[174:175], off
	global_load_dwordx4 v[134:137], v[174:175], off offset:128
	global_load_dwordx4 v[146:149], v[174:175], off offset:256
	global_load_dwordx4 v[158:161], v[174:175], off offset:384
	s_mov_b64 exec, s[98:99]
	v_add_u32_e32 v178, 0x80, v166
	v_cmp_lt_i32_e32 vcc, s33, v178
	s_mov_b64 s[100:101], vcc
	v_cmp_gt_u32_e32 vcc, 0x78, v52
	s_and_b64 s[100:101], s[100:101], vcc
	s_and_b64 exec, s[98:99], s[100:101]
	global_load_dwordx4 v[126:129], v[176:177], off
	global_load_dwordx4 v[138:141], v[176:177], off offset:128
	global_load_dwordx4 v[150:153], v[176:177], off offset:256
	global_load_dwordx4 v[162:165], v[176:177], off offset:384
	s_mov_b64 exec, s[98:99]
	s_barrier
	s_waitcnt vmcnt(0)
	v_lshlrev_b32_e32 v180, 16, v118
	v_and_b32_e32 v181, 0xffff0000, v118
	v_lshlrev_b32_e32 v182, 16, v119
	v_and_b32_e32 v183, 0xffff0000, v119
	v_lshlrev_b32_e32 v184, 16, v120
	v_and_b32_e32 v185, 0xffff0000, v120
	v_lshlrev_b32_e32 v186, 16, v121
	v_and_b32_e32 v187, 0xffff0000, v121
	v_lshlrev_b32_e32 v188, 16, v122
	v_and_b32_e32 v189, 0xffff0000, v122
	v_lshlrev_b32_e32 v190, 16, v123
	v_and_b32_e32 v191, 0xffff0000, v123
	v_lshlrev_b32_e32 v192, 16, v124
	v_and_b32_e32 v193, 0xffff0000, v124
	v_lshlrev_b32_e32 v194, 16, v125
	v_and_b32_e32 v195, 0xffff0000, v125
	v_lshlrev_b32_e32 v196, 16, v126
	v_and_b32_e32 v197, 0xffff0000, v126
	v_lshlrev_b32_e32 v198, 16, v127
	v_and_b32_e32 v199, 0xffff0000, v127
	v_lshlrev_b32_e32 v200, 16, v128
	v_and_b32_e32 v201, 0xffff0000, v128
	v_lshlrev_b32_e32 v202, 16, v129
	v_and_b32_e32 v203, 0xffff0000, v129
	ds_write_b128 v204, v[180:183]
	ds_write_b128 v204, v[184:187] offset:16
	ds_write_b128 v204, v[188:191] offset:16384
	ds_write_b128 v204, v[192:195] offset:16400
	s_mov_b64 s[98:99], exec
	v_cmp_gt_u32_e32 vcc, 0x78, v52
	s_and_b64 exec, s[98:99], vcc
	ds_write_b128 v204, v[196:199] offset:32768
	ds_write_b128 v204, v[200:203] offset:32784
	s_mov_b64 exec, s[98:99]
	v_lshlrev_b32_e32 v2, 1, v40
	v_lshl_or_b32 v36, v55, 7, v2
	v_mov_b32_e32 v37, 0
	v_lshl_add_u64 v[2:3], s[22:23], 0, v[36:37]
	v_add_co_u32_e32 v4, vcc, 0x140000, v2
	s_mov_b64 s[2:3], 0x140000
	s_nop 0
	v_addc_co_u32_e32 v5, vcc, 0, v3, vcc
	v_add_co_u32_e32 v34, vcc, 0x141000, v2
	v_lshl_add_u64 v[42:43], v[2:3], 0, s[2:3]
	s_nop 0
	v_addc_co_u32_e32 v35, vcc, 0, v3, vcc
	global_load_dwordx4 v[14:17], v[42:43], off offset:64
	global_load_dwordx4 v[26:29], v[42:43], off offset:2048
	global_load_dwordx4 v[30:33], v[4:5], off
	global_load_dwordx4 v[10:13], v[42:43], off offset:2112
	global_load_dwordx4 v[22:25], v[34:35], off
	global_load_dwordx4 v[6:9], v[34:35], off offset:64
	global_load_dwordx4 v[18:21], v[34:35], off offset:2048
	s_nop 0
	global_load_dwordx4 v[2:5], v[34:35], off offset:2112
	v_lshlrev_b32_e32 v116, 4, v41
	global_load_dwordx4 v[100:103], v116, s[64:65]
	global_load_dwordx4 v[104:107], v116, s[64:65] offset:64
	global_load_dwordx4 v[108:111], v116, s[64:65] offset:128
	global_load_dwordx4 v[112:115], v116, s[64:65] offset:192
	v_add_u32_e32 v54, s20, v58
	v_add_u32_e32 v56, 1, v54
	v_cmp_gt_i32_e32 vcc, 1, v54
	v_lshlrev_b32_e32 v50, 8, v58
	v_cmp_gt_i32_e64 s[8:9], 1, v56
	v_cmp_lt_i32_e64 s[2:3], 0, v56
	v_cmp_lt_i32_e64 s[6:7], 0, v54
	v_cndmask_b32_e64 v39, 2, 1, vcc
	v_mov_b32_e32 v36, v37
	v_mov_b32_e32 v45, v37
	v_mov_b32_e32 v44, v37
	s_waitcnt lgkmcnt(0)
	s_barrier
	s_and_saveexec_b64 s[20:21], s[2:3]
	s_cbranch_execz .LBB0_377
	v_lshlrev_b32_e32 v34, 6, v1
	v_add3_u32 v34, v50, v34, 0
	v_mov_b32_e32 v44, 0
	v_add_u32_e32 v34, 0xf00, v34
	s_mov_b64 s[22:23], 0
	v_mov_b32_e32 v35, v39
	v_mov_b32_e32 v45, v44
	v_mov_b32_e32 v36, v44
	v_mov_b32_e32 v37, v44

.LBB0_389:
	s_or_b64 exec, exec, s[20:21]
	ds_read_b128 v[46:49], v53 offset:3888
	v_mov_b32_e32 v60, v34
	v_mov_b32_e32 v61, v34
	s_movk_i32 s22, 0x7fff
	s_mov_b32 s23, 0xffff0000
	s_waitcnt lgkmcnt(0)
	v_pk_fma_f32 v[34:35], v[34:35], v[36:37], v[46:47] neg_lo:[0,0,1] neg_hi:[0,0,1]
	v_xor_b32_e32 v49, 0x80000000, v49
	v_bfe_u32 v36, v34, 16, 1
	v_xor_b32_e32 v48, 0x80000000, v48
	v_add3_u32 v34, v34, v36, s22
	v_bfe_u32 v36, v35, 16, 1
	v_pk_fma_f32 v[44:45], v[60:61], v[44:45], v[48:49]
	v_lshrrev_b32_e32 v34, 16, v34
	v_add3_u32 v35, v35, v36, s22
	v_or_b32_e32 v68, s36, v55
	s_movk_i32 s20, 0x90
	v_and_or_b32 v34, v35, s23, v34
	v_bfe_u32 v35, v44, 16, 1
	v_mul_lo_u32 v39, v68, s20
	v_add3_u32 v35, v44, v35, s22
	v_bfe_u32 v36, v45, 16, 1
	v_add_u32_e32 v39, 0, v39
	v_lshrrev_b32_e32 v35, 16, v35
	v_add3_u32 v36, v45, v36, s22
	v_and_or_b32 v35, v36, s23, v35
	v_add_u32_e32 v55, v39, v38
	ds_write_b64 v51, v[34:35] offset:40984
	s_waitcnt lgkmcnt(0)
	s_barrier
	ds_read_b128 v[34:37], v55 offset:40960
	ds_read_b128 v[44:47], v55 offset:41024
	s_waitcnt vmcnt(10) lgkmcnt(1)
	v_mfma_f32_16x16x32_bf16 v[60:63], v[26:29], v[34:37], 0
	v_lshlrev_b32_e32 v26, 4, v41
	v_ashrrev_i32_e32 v69, 31, v68
	s_waitcnt vmcnt(9)
	v_mfma_f32_16x16x32_bf16 v[30:33], v[30:33], v[34:37], 0
	s_movk_i32 s26, 0x1200
	v_mov_b64_e32 v[28:29], s[10:11]
	v_lshl_add_u64 v[38:39], s[0:1], 0, v[68:69]
	s_waitcnt lgkmcnt(0)
	v_mfma_f32_16x16x32_bf16 v[14:17], v[14:17], v[44:47], v[30:33]
	v_mad_u64_u32 v[28:29], s[20:21], v38, s26, v[28:29]
	v_mov_b32_e32 v41, 0
	v_mad_i32_i24 v29, v39, s26, v29
	v_lshl_add_u64 v[38:39], v[28:29], 0, v[40:41]
	s_waitcnt vmcnt(8)
	v_mfma_f32_16x16x32_bf16 v[10:13], v[10:13], v[44:47], v[60:63]
	s_waitcnt vmcnt(0)
	s_nop 0
	v_pk_mul_f32 v[16:17], v[16:17], v[102:103]
	v_pk_mul_f32 v[14:15], v[14:15], v[100:101]
	v_bfe_u32 v29, v16, 16, 1
	v_bfe_u32 v27, v14, 16, 1
	v_bfe_u32 v28, v15, 16, 1
	v_bfe_u32 v30, v17, 16, 1
	v_add3_u32 v14, v14, v27, s22
	v_add3_u32 v16, v16, v29, s22
	v_add3_u32 v15, v15, v28, s22
	v_add3_u32 v17, v17, v30, s22
	v_lshrrev_b32_e32 v14, 16, v14
	v_lshrrev_b32_e32 v16, 16, v16
	v_and_or_b32 v14, v15, s23, v14
	v_and_or_b32 v15, v17, s23, v16
	global_store_dwordx2 v[38:39], v[14:15], off offset:512
	v_mfma_f32_16x16x32_bf16 v[22:25], v[22:25], v[34:37], 0
	v_mov_b32_e32 v27, v41
	v_pk_mul_f32 v[12:13], v[12:13], v[106:107]
	v_pk_mul_f32 v[10:11], v[10:11], v[104:105]
	v_bfe_u32 v16, v12, 16, 1
	v_bfe_u32 v14, v10, 16, 1
	v_bfe_u32 v15, v11, 16, 1
	v_bfe_u32 v17, v13, 16, 1
	v_add3_u32 v10, v10, v14, s22
	v_add3_u32 v12, v12, v16, s22
	v_add3_u32 v11, v11, v15, s22
	v_add3_u32 v13, v13, v17, s22
	v_lshrrev_b32_e32 v10, 16, v10
	v_lshrrev_b32_e32 v12, 16, v12
	v_and_or_b32 v10, v11, s23, v10
	v_and_or_b32 v11, v13, s23, v12
	global_store_dwordx2 v[38:39], v[10:11], off offset:544
	v_mfma_f32_16x16x32_bf16 v[6:9], v[6:9], v[44:47], v[22:25]
	v_mfma_f32_16x16x32_bf16 v[18:21], v[18:21], v[34:37], 0
	v_mfma_f32_16x16x32_bf16 v[2:5], v[2:5], v[44:47], v[18:21]
	s_nop 5
	v_pk_mul_f32 v[8:9], v[8:9], v[110:111]
	v_pk_mul_f32 v[6:7], v[6:7], v[108:109]
	v_bfe_u32 v12, v8, 16, 1
	v_bfe_u32 v10, v6, 16, 1
	v_bfe_u32 v11, v7, 16, 1
	v_bfe_u32 v13, v9, 16, 1
	v_add3_u32 v6, v6, v10, s22
	v_add3_u32 v8, v8, v12, s22
	v_add3_u32 v7, v7, v11, s22
	v_add3_u32 v9, v9, v13, s22
	v_lshrrev_b32_e32 v6, 16, v6
	v_lshrrev_b32_e32 v8, 16, v8
	v_and_or_b32 v6, v7, s23, v6
	v_and_or_b32 v7, v9, s23, v8
	global_store_dwordx2 v[38:39], v[6:7], off offset:576
	v_pk_mul_f32 v[4:5], v[4:5], v[114:115]
	v_pk_mul_f32 v[2:3], v[2:3], v[112:113]
	v_bfe_u32 v8, v4, 16, 1
	v_bfe_u32 v6, v2, 16, 1
	v_bfe_u32 v7, v3, 16, 1
	v_bfe_u32 v9, v5, 16, 1
	v_add3_u32 v2, v2, v6, s22
	v_add3_u32 v4, v4, v8, s22
	v_add3_u32 v3, v3, v7, s22
	v_add3_u32 v5, v5, v9, s22
	v_lshrrev_b32_e32 v2, 16, v2
	v_lshrrev_b32_e32 v4, 16, v4
	v_and_or_b32 v2, v3, s23, v2
	v_and_or_b32 v3, v5, s23, v4
	global_store_dwordx2 v[38:39], v[2:3], off offset:608
	s_barrier
	v_lshlrev_b32_e32 v180, 16, v130
	v_and_b32_e32 v181, 0xffff0000, v130
	v_lshlrev_b32_e32 v182, 16, v131
	v_and_b32_e32 v183, 0xffff0000, v131
	v_lshlrev_b32_e32 v184, 16, v132
	v_and_b32_e32 v185, 0xffff0000, v132
	v_lshlrev_b32_e32 v186, 16, v133
	v_and_b32_e32 v187, 0xffff0000, v133
	v_lshlrev_b32_e32 v188, 16, v134
	v_and_b32_e32 v189, 0xffff0000, v134
	v_lshlrev_b32_e32 v190, 16, v135
	v_and_b32_e32 v191, 0xffff0000, v135
	v_lshlrev_b32_e32 v192, 16, v136
	v_and_b32_e32 v193, 0xffff0000, v136
	v_lshlrev_b32_e32 v194, 16, v137
	v_and_b32_e32 v195, 0xffff0000, v137
	v_lshlrev_b32_e32 v196, 16, v138
	v_and_b32_e32 v197, 0xffff0000, v138
	v_lshlrev_b32_e32 v198, 16, v139
	v_and_b32_e32 v199, 0xffff0000, v139
	v_lshlrev_b32_e32 v200, 16, v140
	v_and_b32_e32 v201, 0xffff0000, v140
	v_lshlrev_b32_e32 v202, 16, v141
	v_and_b32_e32 v203, 0xffff0000, v141
	ds_write_b128 v204, v[180:183]
	ds_write_b128 v204, v[184:187] offset:16
	ds_write_b128 v204, v[188:191] offset:16384
	ds_write_b128 v204, v[192:195] offset:16400
	s_mov_b64 s[98:99], exec
	v_cmp_gt_u32_e32 vcc, 0x78, v52
	s_and_b64 exec, s[98:99], vcc
	ds_write_b128 v204, v[196:199] offset:32768
	ds_write_b128 v204, v[200:203] offset:32784
	s_mov_b64 exec, s[98:99]
	v_add_co_u32_e32 v2, vcc, 0x2000, v42
	v_lshl_add_u64 v[40:41], s[64:65], 0, v[26:27]
	s_nop 0
	v_addc_co_u32_e32 v3, vcc, 0, v43, vcc
	global_load_dwordx4 v[18:21], v[2:3], off
	global_load_dwordx4 v[14:17], v[2:3], off offset:64
	global_load_dwordx4 v[22:25], v[2:3], off offset:2048
	global_load_dwordx4 v[10:13], v[2:3], off offset:2112
	v_add_co_u32_e32 v2, vcc, 0x3000, v42
	v_max_i32_e32 v34, 0, v54
	s_nop 0
	v_addc_co_u32_e32 v3, vcc, 0, v43, vcc
	global_load_dwordx4 v[26:29], v[2:3], off
	global_load_dwordx4 v[6:9], v[2:3], off offset:64
	global_load_dwordx4 v[30:33], v[2:3], off offset:2048
	s_nop 0
	global_load_dwordx4 v[2:5], v[2:3], off offset:2112
	global_load_dwordx4 v[100:103], v[40:41], off offset:256
	global_load_dwordx4 v[104:107], v[40:41], off offset:320
	global_load_dwordx4 v[108:111], v[40:41], off offset:384
	global_load_dwordx4 v[112:115], v[40:41], off offset:448
	v_add_u32_e32 v60, 1, v34
	v_mov_b32_e32 v45, 0
	v_min_u32_e32 v46, 4, v60
	v_mov_b32_e32 v44, v45
	v_mov_b32_e32 v37, v45
	v_mov_b32_e32 v36, v45
	s_waitcnt lgkmcnt(0)
	s_barrier
	s_and_saveexec_b64 s[20:21], s[2:3]
	s_cbranch_execz .LBB0_398
	v_lshlrev_b32_e32 v34, 6, v1
	v_add3_u32 v34, v50, v34, 0
	v_mov_b32_e32 v36, 0
	v_add_u32_e32 v34, 0xf00, v34
	s_mov_b64 s[22:23], 0
	v_mov_b32_e32 v35, v46
	v_mov_b32_e32 v37, v36
	v_mov_b32_e32 v44, v36
	v_mov_b32_e32 v45, v36

.LBB0_410:
	s_or_b64 exec, exec, s[20:21]
	ds_read_b128 v[46:49], v53 offset:3888
	v_mov_b32_e32 v62, v34
	v_mov_b32_e32 v63, v34
	s_movk_i32 s20, 0x7fff
	s_mov_b32 s21, 0xffff0000
	s_waitcnt lgkmcnt(0)
	v_xor_b32_e32 v49, 0x80000000, v49
	v_xor_b32_e32 v48, 0x80000000, v48
	v_pk_fma_f32 v[34:35], v[34:35], v[36:37], v[46:47] neg_lo:[0,0,1] neg_hi:[0,0,1]
	v_pk_fma_f32 v[36:37], v[62:63], v[44:45], v[48:49]
	v_bfe_u32 v44, v34, 16, 1
	v_add3_u32 v34, v34, v44, s20
	v_bfe_u32 v44, v35, 16, 1
	v_lshrrev_b32_e32 v34, 16, v34
	v_add3_u32 v35, v35, v44, s20
	v_and_or_b32 v34, v35, s21, v34
	v_bfe_u32 v35, v36, 16, 1
	v_add3_u32 v35, v36, v35, s20
	v_bfe_u32 v36, v37, 16, 1
	v_lshrrev_b32_e32 v35, 16, v35
	v_add3_u32 v36, v37, v36, s20
	v_and_or_b32 v35, v36, s21, v35
	ds_write_b64 v51, v[34:35] offset:40984
	s_waitcnt lgkmcnt(0)
	s_barrier
	ds_read_b128 v[34:37], v55 offset:40960
	ds_read_b128 v[44:47], v55 offset:41024
	s_waitcnt vmcnt(11) lgkmcnt(1)
	v_mfma_f32_16x16x32_bf16 v[18:21], v[18:21], v[34:37], 0
	s_waitcnt vmcnt(9)
	v_mfma_f32_16x16x32_bf16 v[22:25], v[22:25], v[34:37], 0
	s_waitcnt vmcnt(7)
	v_mfma_f32_16x16x32_bf16 v[26:29], v[26:29], v[34:37], 0
	s_waitcnt vmcnt(5)
	v_mfma_f32_16x16x32_bf16 v[30:33], v[30:33], v[34:37], 0
	s_waitcnt lgkmcnt(0)
	v_mfma_f32_16x16x32_bf16 v[14:17], v[14:17], v[44:47], v[18:21]
	v_mfma_f32_16x16x32_bf16 v[10:13], v[10:13], v[44:47], v[22:25]
	v_mfma_f32_16x16x32_bf16 v[6:9], v[6:9], v[44:47], v[26:29]
	s_waitcnt vmcnt(0)
	s_nop 4
	v_pk_mul_f32 v[16:17], v[16:17], v[102:103]
	v_pk_mul_f32 v[14:15], v[14:15], v[100:101]
	v_bfe_u32 v20, v16, 16, 1
	v_bfe_u32 v18, v14, 16, 1
	v_bfe_u32 v19, v15, 16, 1
	v_bfe_u32 v21, v17, 16, 1
	v_add3_u32 v14, v14, v18, s20
	v_add3_u32 v16, v16, v20, s20
	v_add3_u32 v15, v15, v19, s20
	v_add3_u32 v17, v17, v21, s20
	v_lshrrev_b32_e32 v14, 16, v14
	v_lshrrev_b32_e32 v16, 16, v16
	v_and_or_b32 v14, v15, s21, v14
	v_and_or_b32 v15, v17, s21, v16
	global_store_dwordx2 v[38:39], v[14:15], off offset:640
	v_mfma_f32_16x16x32_bf16 v[2:5], v[2:5], v[44:47], v[30:33]
	v_pk_mul_f32 v[12:13], v[12:13], v[106:107]
	v_pk_mul_f32 v[10:11], v[10:11], v[104:105]
	v_bfe_u32 v16, v12, 16, 1
	v_bfe_u32 v14, v10, 16, 1
	v_bfe_u32 v15, v11, 16, 1
	v_bfe_u32 v17, v13, 16, 1
	v_add3_u32 v10, v10, v14, s20
	v_add3_u32 v12, v12, v16, s20
	v_add3_u32 v11, v11, v15, s20
	v_add3_u32 v13, v13, v17, s20
	v_lshrrev_b32_e32 v10, 16, v10
	v_lshrrev_b32_e32 v12, 16, v12
	v_and_or_b32 v10, v11, s21, v10
	v_and_or_b32 v11, v13, s21, v12
	global_store_dwordx2 v[38:39], v[10:11], off offset:672
	v_pk_mul_f32 v[8:9], v[8:9], v[110:111]
	v_pk_mul_f32 v[6:7], v[6:7], v[108:109]
	v_bfe_u32 v12, v8, 16, 1
	v_bfe_u32 v10, v6, 16, 1
	v_bfe_u32 v11, v7, 16, 1
	v_bfe_u32 v13, v9, 16, 1
	v_add3_u32 v6, v6, v10, s20
	v_add3_u32 v8, v8, v12, s20
	v_add3_u32 v7, v7, v11, s20
	v_add3_u32 v9, v9, v13, s20
	v_lshrrev_b32_e32 v6, 16, v6
	v_lshrrev_b32_e32 v8, 16, v8
	v_and_or_b32 v6, v7, s21, v6
	v_and_or_b32 v7, v9, s21, v8
	global_store_dwordx2 v[38:39], v[6:7], off offset:704
	v_pk_mul_f32 v[4:5], v[4:5], v[114:115]
	v_pk_mul_f32 v[2:3], v[2:3], v[112:113]
	v_bfe_u32 v8, v4, 16, 1
	v_bfe_u32 v6, v2, 16, 1
	v_bfe_u32 v7, v3, 16, 1
	v_bfe_u32 v9, v5, 16, 1
	v_add3_u32 v2, v2, v6, s20
	v_add3_u32 v4, v4, v8, s20
	v_add3_u32 v3, v3, v7, s20
	v_add3_u32 v5, v5, v9, s20
	v_lshrrev_b32_e32 v2, 16, v2
	v_lshrrev_b32_e32 v4, 16, v4
	v_and_or_b32 v2, v3, s21, v2
	v_and_or_b32 v3, v5, s21, v4
	global_store_dwordx2 v[38:39], v[2:3], off offset:736
	s_barrier
	v_lshlrev_b32_e32 v180, 16, v142
	v_and_b32_e32 v181, 0xffff0000, v142
	v_lshlrev_b32_e32 v182, 16, v143
	v_and_b32_e32 v183, 0xffff0000, v143
	v_lshlrev_b32_e32 v184, 16, v144
	v_and_b32_e32 v185, 0xffff0000, v144
	v_lshlrev_b32_e32 v186, 16, v145
	v_and_b32_e32 v187, 0xffff0000, v145
	v_lshlrev_b32_e32 v188, 16, v146
	v_and_b32_e32 v189, 0xffff0000, v146
	v_lshlrev_b32_e32 v190, 16, v147
	v_and_b32_e32 v191, 0xffff0000, v147
	v_lshlrev_b32_e32 v192, 16, v148
	v_and_b32_e32 v193, 0xffff0000, v148
	v_lshlrev_b32_e32 v194, 16, v149
	v_and_b32_e32 v195, 0xffff0000, v149
	v_lshlrev_b32_e32 v196, 16, v150
	v_and_b32_e32 v197, 0xffff0000, v150
	v_lshlrev_b32_e32 v198, 16, v151
	v_and_b32_e32 v199, 0xffff0000, v151
	v_lshlrev_b32_e32 v200, 16, v152
	v_and_b32_e32 v201, 0xffff0000, v152
	v_lshlrev_b32_e32 v202, 16, v153
	v_and_b32_e32 v203, 0xffff0000, v153
	ds_write_b128 v204, v[180:183]
	ds_write_b128 v204, v[184:187] offset:16
	ds_write_b128 v204, v[188:191] offset:16384
	ds_write_b128 v204, v[192:195] offset:16400
	s_mov_b64 s[98:99], exec
	v_cmp_gt_u32_e32 vcc, 0x78, v52
	s_and_b64 exec, s[98:99], vcc
	ds_write_b128 v204, v[196:199] offset:32768
	ds_write_b128 v204, v[200:203] offset:32784
	s_mov_b64 exec, s[98:99]
	v_add_co_u32_e32 v2, vcc, 0x4000, v42
	s_nop 1
	v_addc_co_u32_e32 v3, vcc, 0, v43, vcc
	global_load_dwordx4 v[18:21], v[2:3], off
	global_load_dwordx4 v[14:17], v[2:3], off offset:64
	global_load_dwordx4 v[22:25], v[2:3], off offset:2048
	global_load_dwordx4 v[10:13], v[2:3], off offset:2112
	v_add_co_u32_e32 v2, vcc, 0x5000, v42
	s_nop 1
	v_addc_co_u32_e32 v3, vcc, 0, v43, vcc
	global_load_dwordx4 v[26:29], v[2:3], off
	global_load_dwordx4 v[6:9], v[2:3], off offset:64
	global_load_dwordx4 v[30:33], v[2:3], off offset:2048
	s_nop 0
	global_load_dwordx4 v[2:5], v[2:3], off offset:2112
	global_load_dwordx4 v[100:103], v[40:41], off offset:512
	global_load_dwordx4 v[104:107], v[40:41], off offset:576
	global_load_dwordx4 v[108:111], v[40:41], off offset:640
	global_load_dwordx4 v[112:115], v[40:41], off offset:704
	s_waitcnt lgkmcnt(0)
	s_barrier
	s_and_saveexec_b64 s[20:21], s[8:9]
	s_xor_b64 s[20:21], exec, s[20:21]
	ds_read_b128 v[34:37], v53 offset:3840
	s_or_saveexec_b64 s[20:21], s[20:21]
	v_lshl_add_u32 v59, v59, 2, 0
	v_add_u32_e32 v44, 15, v58
	v_mov_b32_e32 v46, 0
	v_lshl_add_u32 v58, v44, 8, v59
	v_mov_b32_e32 v47, 0
	v_mov_b32_e32 v48, 0
	v_mov_b32_e32 v49, 0
	s_xor_b64 exec, exec, s[20:21]
	s_cbranch_execz .LBB0_433
	s_waitcnt lgkmcnt(0)
	ds_read_b128 v[34:37], v58
	s_waitcnt lgkmcnt(0)
	v_pk_add_f32 v[48:49], v[36:37], 0 op_sel_hi:[1,0]
	v_pk_add_f32 v[46:47], v[34:35], 0 op_sel_hi:[1,0]
	s_and_saveexec_b64 s[22:23], s[6:7]
	s_cbranch_execz .LBB0_432
	v_add_u32_e32 v44, v59, v50
	ds_read_b128 v[62:65], v44 offset:3584
	v_cmp_ne_u32_e32 vcc, 2, v60
	s_waitcnt lgkmcnt(0)
	v_pk_add_f32 v[48:49], v[48:49], v[64:65]
	v_pk_add_f32 v[46:47], v[46:47], v[62:63]
	s_and_saveexec_b64 s[24:25], vcc
	s_cbranch_execz .LBB0_431
	ds_read_b128 v[62:65], v44 offset:3328
	v_cmp_ne_u32_e32 vcc, 3, v60
	s_waitcnt lgkmcnt(0)
	v_pk_add_f32 v[48:49], v[48:49], v[64:65]
	v_pk_add_f32 v[46:47], v[46:47], v[62:63]
	s_and_saveexec_b64 s[26:27], vcc
	s_cbranch_execz .LBB0_430
	ds_read_b128 v[62:65], v44 offset:3072
	v_cmp_ne_u32_e32 vcc, 4, v60
	s_waitcnt lgkmcnt(0)
	v_pk_add_f32 v[48:49], v[48:49], v[64:65]
	v_pk_add_f32 v[46:47], v[46:47], v[62:63]
	s_and_saveexec_b64 s[28:29], vcc
	s_cbranch_execz .LBB0_429
	ds_read_b128 v[62:65], v44 offset:2816
	v_cmp_ne_u32_e32 vcc, 5, v60
	s_waitcnt lgkmcnt(0)
	v_pk_add_f32 v[48:49], v[48:49], v[64:65]
	v_pk_add_f32 v[46:47], v[46:47], v[62:63]
	s_and_saveexec_b64 s[30:31], vcc
	s_cbranch_execz .LBB0_428
	ds_read_b128 v[62:65], v44 offset:2560
	v_cmp_ne_u32_e32 vcc, 6, v60
	s_waitcnt lgkmcnt(0)
	v_pk_add_f32 v[48:49], v[48:49], v[64:65]
	v_pk_add_f32 v[46:47], v[46:47], v[62:63]
	s_and_saveexec_b64 s[34:35], vcc
	s_cbranch_execz .LBB0_427
	ds_read_b128 v[62:65], v44 offset:2304
	v_cmp_ne_u32_e32 vcc, 7, v60
	s_waitcnt lgkmcnt(0)
	v_pk_add_f32 v[48:49], v[48:49], v[64:65]
	v_pk_add_f32 v[46:47], v[46:47], v[62:63]
	s_and_saveexec_b64 s[36:37], vcc
	s_cbranch_execz .LBB0_426
	ds_read_b128 v[62:65], v44 offset:2048
	s_waitcnt lgkmcnt(0)
	v_pk_add_f32 v[48:49], v[48:49], v[64:65]
	v_pk_add_f32 v[46:47], v[46:47], v[62:63]

.LBB0_487:
	s_or_b64 exec, exec, s[8:9]
	s_waitcnt lgkmcnt(0)
	v_pk_fma_f32 v[34:35], v[44:45], v[46:47], v[34:35] neg_lo:[0,0,1] neg_hi:[0,0,1]
	v_mov_b32_e32 v58, v44
	v_mov_b32_e32 v59, v44
	v_bfe_u32 v44, v34, 16, 1
	s_movk_i32 s6, 0x7fff
	v_xor_b32_e32 v37, 0x80000000, v37
	v_xor_b32_e32 v36, 0x80000000, v36
	v_add3_u32 v34, v34, v44, s6
	v_bfe_u32 v44, v35, 16, 1
	v_pk_fma_f32 v[36:37], v[58:59], v[48:49], v[36:37]
	v_lshrrev_b32_e32 v34, 16, v34
	v_add3_u32 v35, v35, v44, s6
	s_mov_b32 s7, 0xffff0000
	v_and_or_b32 v34, v35, s7, v34
	v_bfe_u32 v35, v36, 16, 1
	v_add3_u32 v35, v36, v35, s6
	v_bfe_u32 v36, v37, 16, 1
	v_lshrrev_b32_e32 v35, 16, v35
	v_add3_u32 v36, v37, v36, s6
	v_and_or_b32 v35, v36, s7, v35
	ds_write_b64 v51, v[34:35] offset:40984
	s_waitcnt lgkmcnt(0)
	s_barrier
	ds_read_b128 v[34:37], v55 offset:40960
	ds_read_b128 v[44:47], v55 offset:41024
	s_waitcnt vmcnt(11) lgkmcnt(1)
	v_mfma_f32_16x16x32_bf16 v[18:21], v[18:21], v[34:37], 0
	s_waitcnt vmcnt(9)
	v_mfma_f32_16x16x32_bf16 v[22:25], v[22:25], v[34:37], 0
	s_waitcnt vmcnt(7)
	v_mfma_f32_16x16x32_bf16 v[26:29], v[26:29], v[34:37], 0
	s_waitcnt vmcnt(5)
	v_mfma_f32_16x16x32_bf16 v[30:33], v[30:33], v[34:37], 0
	s_waitcnt lgkmcnt(0)
	v_mfma_f32_16x16x32_bf16 v[14:17], v[14:17], v[44:47], v[18:21]
	v_mfma_f32_16x16x32_bf16 v[10:13], v[10:13], v[44:47], v[22:25]
	v_mfma_f32_16x16x32_bf16 v[6:9], v[6:9], v[44:47], v[26:29]
	s_waitcnt vmcnt(0)
	s_nop 4
	v_pk_mul_f32 v[16:17], v[16:17], v[102:103]
	v_pk_mul_f32 v[14:15], v[14:15], v[100:101]
	v_bfe_u32 v20, v16, 16, 1
	v_bfe_u32 v18, v14, 16, 1
	v_bfe_u32 v19, v15, 16, 1
	v_bfe_u32 v21, v17, 16, 1
	v_add3_u32 v14, v14, v18, s6
	v_add3_u32 v16, v16, v20, s6
	v_add3_u32 v15, v15, v19, s6
	v_add3_u32 v17, v17, v21, s6
	v_lshrrev_b32_e32 v14, 16, v14
	v_lshrrev_b32_e32 v16, 16, v16
	v_and_or_b32 v14, v15, s7, v14
	v_and_or_b32 v15, v17, s7, v16
	global_store_dwordx2 v[38:39], v[14:15], off offset:768
	v_mfma_f32_16x16x32_bf16 v[2:5], v[2:5], v[44:47], v[30:33]
	v_pk_mul_f32 v[12:13], v[12:13], v[106:107]
	v_pk_mul_f32 v[10:11], v[10:11], v[104:105]
	v_bfe_u32 v16, v12, 16, 1
	v_bfe_u32 v14, v10, 16, 1
	v_bfe_u32 v15, v11, 16, 1
	v_bfe_u32 v17, v13, 16, 1
	v_add3_u32 v10, v10, v14, s6
	v_add3_u32 v12, v12, v16, s6
	v_add3_u32 v11, v11, v15, s6
	v_add3_u32 v13, v13, v17, s6
	v_lshrrev_b32_e32 v10, 16, v10
	v_lshrrev_b32_e32 v12, 16, v12
	v_and_or_b32 v10, v11, s7, v10
	v_and_or_b32 v11, v13, s7, v12
	global_store_dwordx2 v[38:39], v[10:11], off offset:800
	v_pk_mul_f32 v[8:9], v[8:9], v[110:111]
	v_pk_mul_f32 v[6:7], v[6:7], v[108:109]
	v_bfe_u32 v12, v8, 16, 1
	v_bfe_u32 v10, v6, 16, 1
	v_bfe_u32 v11, v7, 16, 1
	v_bfe_u32 v13, v9, 16, 1
	v_add3_u32 v6, v6, v10, s6
	v_add3_u32 v8, v8, v12, s6
	v_add3_u32 v7, v7, v11, s6
	v_add3_u32 v9, v9, v13, s6
	v_lshrrev_b32_e32 v6, 16, v6
	v_lshrrev_b32_e32 v8, 16, v8
	v_and_or_b32 v6, v7, s7, v6
	v_and_or_b32 v7, v9, s7, v8
	global_store_dwordx2 v[38:39], v[6:7], off offset:832
	v_pk_mul_f32 v[4:5], v[4:5], v[114:115]
	v_pk_mul_f32 v[2:3], v[2:3], v[112:113]
	v_bfe_u32 v8, v4, 16, 1
	v_bfe_u32 v6, v2, 16, 1
	v_bfe_u32 v7, v3, 16, 1
	v_bfe_u32 v9, v5, 16, 1
	v_add3_u32 v2, v2, v6, s6
	v_add3_u32 v4, v4, v8, s6
	v_add3_u32 v3, v3, v7, s6
	v_add3_u32 v5, v5, v9, s6
	v_lshrrev_b32_e32 v2, 16, v2
	v_lshrrev_b32_e32 v4, 16, v4
	v_and_or_b32 v2, v3, s7, v2
	v_and_or_b32 v3, v5, s7, v4
	global_store_dwordx2 v[38:39], v[2:3], off offset:864
	s_barrier
	v_lshlrev_b32_e32 v180, 16, v154
	v_and_b32_e32 v181, 0xffff0000, v154
	v_lshlrev_b32_e32 v182, 16, v155
	v_and_b32_e32 v183, 0xffff0000, v155
	v_lshlrev_b32_e32 v184, 16, v156
	v_and_b32_e32 v185, 0xffff0000, v156
	v_lshlrev_b32_e32 v186, 16, v157
	v_and_b32_e32 v187, 0xffff0000, v157
	v_lshlrev_b32_e32 v188, 16, v158
	v_and_b32_e32 v189, 0xffff0000, v158
	v_lshlrev_b32_e32 v190, 16, v159
	v_and_b32_e32 v191, 0xffff0000, v159
	v_lshlrev_b32_e32 v192, 16, v160
	v_and_b32_e32 v193, 0xffff0000, v160
	v_lshlrev_b32_e32 v194, 16, v161
	v_and_b32_e32 v195, 0xffff0000, v161
	v_lshlrev_b32_e32 v196, 16, v162
	v_and_b32_e32 v197, 0xffff0000, v162
	v_lshlrev_b32_e32 v198, 16, v163
	v_and_b32_e32 v199, 0xffff0000, v163
	v_lshlrev_b32_e32 v200, 16, v164
	v_and_b32_e32 v201, 0xffff0000, v164
	v_lshlrev_b32_e32 v202, 16, v165
	v_and_b32_e32 v203, 0xffff0000, v165
	ds_write_b128 v204, v[180:183]
	ds_write_b128 v204, v[184:187] offset:16
	ds_write_b128 v204, v[188:191] offset:16384
	ds_write_b128 v204, v[192:195] offset:16400
	s_mov_b64 s[98:99], exec
	v_cmp_gt_u32_e32 vcc, 0x78, v52
	s_and_b64 exec, s[98:99], vcc
	ds_write_b128 v204, v[196:199] offset:32768
	ds_write_b128 v204, v[200:203] offset:32784
	s_mov_b64 exec, s[98:99]
	v_add_co_u32_e32 v2, vcc, 0x6000, v42
	v_min_u32_e32 v44, 16, v60
	s_nop 0
	v_addc_co_u32_e32 v3, vcc, 0, v43, vcc
	v_add_co_u32_e32 v34, vcc, 0x7000, v42
	global_load_dwordx4 v[18:21], v[2:3], off
	global_load_dwordx4 v[14:17], v[2:3], off offset:64
	global_load_dwordx4 v[22:25], v[2:3], off offset:2048
	global_load_dwordx4 v[10:13], v[2:3], off offset:2112
	v_addc_co_u32_e32 v35, vcc, 0, v43, vcc
	global_load_dwordx4 v[26:29], v[34:35], off
	global_load_dwordx4 v[6:9], v[34:35], off offset:64
	global_load_dwordx4 v[30:33], v[34:35], off offset:2048
	global_load_dwordx4 v[2:5], v[34:35], off offset:2112
	global_load_dwordx4 v[100:103], v[40:41], off offset:768
	global_load_dwordx4 v[104:107], v[40:41], off offset:832
	global_load_dwordx4 v[108:111], v[40:41], off offset:896
	global_load_dwordx4 v[112:115], v[40:41], off offset:960
	v_mov_b32_e32 v43, 0
	v_mov_b32_e32 v42, 0
	v_mov_b32_e32 v37, 0
	v_mov_b32_e32 v36, 0
	s_waitcnt lgkmcnt(0)
	s_barrier
	s_and_saveexec_b64 s[0:1], s[2:3]
	s_cbranch_execz .LBB0_502
	v_mov_b32_e32 v36, 0
	v_cmp_lt_i32_e32 vcc, 6, v54
	s_mov_b32 s8, 0
	v_mov_b32_e32 v37, v36
	v_mov_b32_e32 v42, v36
	v_mov_b32_e32 v43, v36
	v_mov_b32_e32 v34, v36
	s_and_saveexec_b64 s[4:5], vcc
	s_cbranch_execz .LBB0_497
	v_lshlrev_b32_e32 v35, 6, v1
	v_add3_u32 v35, v50, v35, 0
	v_mov_b32_e32 v36, 0
	v_and_b32_e32 v34, 24, v44
	v_add_u32_e32 v35, 0x800, v35
	s_mov_b64 s[6:7], 0
	v_mov_b32_e32 v37, v36
	v_mov_b32_e32 v42, v36
	v_mov_b32_e32 v43, v36

.LBB0_532:
	s_or_b64 exec, exec, s[0:1]
	ds_read_b128 v[44:47], v53 offset:3888
	v_mov_b32_e32 v48, v34
	v_mov_b32_e32 v49, v34
	s_movk_i32 s0, 0x7fff
	s_mov_b32 s1, 0xffff0000
	s_waitcnt lgkmcnt(0)
	v_pk_fma_f32 v[34:35], v[34:35], v[36:37], v[44:45] neg_lo:[0,0,1] neg_hi:[0,0,1]
	v_xor_b32_e32 v47, 0x80000000, v47
	v_bfe_u32 v1, v34, 16, 1
	v_xor_b32_e32 v46, 0x80000000, v46
	v_add3_u32 v1, v34, v1, s0
	v_bfe_u32 v34, v35, 16, 1
	v_pk_fma_f32 v[36:37], v[48:49], v[42:43], v[46:47]
	v_lshrrev_b32_e32 v1, 16, v1
	v_add3_u32 v34, v35, v34, s0
	v_and_or_b32 v34, v34, s1, v1
	v_bfe_u32 v1, v36, 16, 1
	v_add3_u32 v1, v36, v1, s0
	v_bfe_u32 v35, v37, 16, 1
	v_lshrrev_b32_e32 v1, 16, v1
	v_add3_u32 v35, v37, v35, s0
	v_and_or_b32 v35, v35, s1, v1
	ds_write_b64 v51, v[34:35] offset:40984
	s_waitcnt lgkmcnt(0)
	s_barrier
	ds_read_b128 v[34:37], v55 offset:40960
	ds_read_b128 v[42:45], v55 offset:41024
	s_waitcnt vmcnt(11) lgkmcnt(1)
	v_mfma_f32_16x16x32_bf16 v[18:21], v[18:21], v[34:37], 0
	s_mov_b32 s3, 0
	s_waitcnt vmcnt(9)
	v_mfma_f32_16x16x32_bf16 v[22:25], v[22:25], v[34:37], 0
	s_waitcnt vmcnt(7)
	v_mfma_f32_16x16x32_bf16 v[26:29], v[26:29], v[34:37], 0
	s_waitcnt vmcnt(5)
	v_mfma_f32_16x16x32_bf16 v[30:33], v[30:33], v[34:37], 0
	s_waitcnt lgkmcnt(0)
	v_mfma_f32_16x16x32_bf16 v[14:17], v[14:17], v[42:45], v[18:21]
	v_mfma_f32_16x16x32_bf16 v[10:13], v[10:13], v[42:45], v[22:25]
	v_mfma_f32_16x16x32_bf16 v[6:9], v[6:9], v[42:45], v[26:29]
	s_waitcnt vmcnt(0)
	s_nop 4
	v_pk_mul_f32 v[16:17], v[16:17], v[102:103]
	v_pk_mul_f32 v[14:15], v[14:15], v[100:101]
	v_bfe_u32 v19, v16, 16, 1
	v_bfe_u32 v1, v14, 16, 1
	v_bfe_u32 v18, v15, 16, 1
	v_bfe_u32 v20, v17, 16, 1
	v_add3_u32 v1, v14, v1, s0
	v_add3_u32 v14, v15, v18, s0
	v_add3_u32 v15, v16, v19, s0
	v_add3_u32 v16, v17, v20, s0
	v_lshrrev_b32_e32 v1, 16, v1
	v_lshrrev_b32_e32 v15, 16, v15
	v_and_or_b32 v14, v14, s1, v1
	v_and_or_b32 v15, v16, s1, v15
	global_store_dwordx2 v[38:39], v[14:15], off offset:896
	v_mfma_f32_16x16x32_bf16 v[2:5], v[2:5], v[42:45], v[30:33]
	v_pk_mul_f32 v[12:13], v[12:13], v[106:107]
	v_pk_mul_f32 v[10:11], v[10:11], v[104:105]
	v_bfe_u32 v15, v12, 16, 1
	v_bfe_u32 v1, v10, 16, 1
	v_bfe_u32 v14, v11, 16, 1
	v_bfe_u32 v16, v13, 16, 1
	v_add3_u32 v1, v10, v1, s0
	v_add3_u32 v10, v11, v14, s0
	v_add3_u32 v11, v12, v15, s0
	v_add3_u32 v12, v13, v16, s0
	v_lshrrev_b32_e32 v1, 16, v1
	v_lshrrev_b32_e32 v11, 16, v11
	v_and_or_b32 v10, v10, s1, v1
	v_and_or_b32 v11, v12, s1, v11
	global_store_dwordx2 v[38:39], v[10:11], off offset:928
	v_pk_mul_f32 v[8:9], v[8:9], v[110:111]
	v_pk_mul_f32 v[6:7], v[6:7], v[108:109]
	v_bfe_u32 v11, v8, 16, 1
	v_bfe_u32 v1, v6, 16, 1
	v_bfe_u32 v10, v7, 16, 1
	v_bfe_u32 v12, v9, 16, 1
	v_add3_u32 v1, v6, v1, s0
	v_add3_u32 v6, v7, v10, s0
	v_add3_u32 v7, v8, v11, s0
	v_add3_u32 v8, v9, v12, s0
	v_lshrrev_b32_e32 v1, 16, v1
	v_lshrrev_b32_e32 v7, 16, v7
	v_and_or_b32 v6, v6, s1, v1
	v_and_or_b32 v7, v8, s1, v7
	global_store_dwordx2 v[38:39], v[6:7], off offset:960
	v_pk_mul_f32 v[4:5], v[4:5], v[114:115]
	v_pk_mul_f32 v[2:3], v[2:3], v[112:113]
	v_bfe_u32 v7, v4, 16, 1
	v_bfe_u32 v1, v2, 16, 1
	v_bfe_u32 v6, v3, 16, 1
	v_bfe_u32 v8, v5, 16, 1
	v_add3_u32 v1, v2, v1, s0
	v_add3_u32 v2, v3, v6, s0
	v_add3_u32 v3, v4, v7, s0
	v_add3_u32 v4, v5, v8, s0
	v_lshrrev_b32_e32 v1, 16, v1
	v_lshrrev_b32_e32 v3, 16, v3
	v_and_or_b32 v2, v2, s1, v1
	v_and_or_b32 v3, v4, s1, v3
	global_store_dwordx2 v[38:39], v[2:3], off offset:992
	s_barrier
	s_waitcnt vmcnt(0)
	s_barrier
	s_mov_b64 s[0:1], exec
	v_readlane_b32 s4, v254, 2
	v_readlane_b32 s5, v254, 3
	s_and_b64 s[4:5], s[0:1], s[4:5]
	s_mov_b64 exec, s[4:5]
	s_cbranch_execz .LBB0_584
	s_mov_b32 s2, 0
	s_lshl_b64 s[2:3], s[2:3], 2
	v_readlane_b32 s4, v254, 0
	v_readlane_b32 s5, v254, 1
	s_add_u32 s2, s4, s2
	s_addc_u32 s3, s5, s3
	s_add_i32 s4, 0, 0x20160
	v_mov_b32_e32 v1, s4
	s_waitcnt vmcnt(0) expcnt(0) lgkmcnt(0)
	ds_read_b32 v3, v1
	s_add_i32 s4, 0, 0x20164
	v_mov_b32_e32 v1, s4
	ds_read_b32 v1, v1
	s_waitcnt lgkmcnt(1)
	v_cmp_ne_u32_e32 vcc, 0, v3
	s_cbranch_vccnz .LBB0_548
	v_readlane_b32 s4, v254, 20
	v_readlane_b32 s5, v254, 21
	s_load_dwordx2 s[8:9], s[4:5], 0x4
	s_add_u32 s4, s2, 0x1000
	s_addc_u32 s5, s3, 0
	s_add_u32 s6, s2, 0x1100
	s_addc_u32 s7, s3, 0
	v_readlane_b32 s10, v254, 22
	s_waitcnt lgkmcnt(0)
	s_mul_i32 s26, s8, s10
	s_add_u32 s8, s2, 0x1200
	s_mul_i32 s26, s26, s9
	s_addc_u32 s9, s3, 0
	s_add_u32 s10, s2, 0x1300
	s_addc_u32 s11, s3, 0
	s_mov_b32 s27, 1
	v_mov_b32_e32 v17, 0
	s_branch .LBB0_536

.LBB0_981:
	s_lshr_b32 s2, s21, 25
	s_add_i32 s2, s20, s2
	s_and_b32 s2, s2, 0x1ffff80
	s_sub_i32 s2, s20, s2
	s_lshl_b32 s12, s2, 7
	s_movk_i32 s2, 0x478
	s_lshl_b64 s[0:1], s[20:21], 7
	s_not_b32 s28, s12
	v_cmp_gt_i32_e64 s[4:5], s2, v52
	v_lshlrev_b32_e32 v57, 3, v52
	v_mov_b32_e32 v118, 0
	v_mov_b32_e32 v119, 0
	v_mov_b32_e32 v120, 0
	v_mov_b32_e32 v121, 0
	v_mov_b32_e32 v122, 0
	v_mov_b32_e32 v123, 0
	v_mov_b32_e32 v124, 0
	v_mov_b32_e32 v125, 0
	v_mov_b32_e32 v126, 0
	v_mov_b32_e32 v127, 0
	v_mov_b32_e32 v128, 0
	v_mov_b32_e32 v129, 0
	v_mov_b32_e32 v130, 0
	v_mov_b32_e32 v131, 0
	v_mov_b32_e32 v132, 0
	v_mov_b32_e32 v133, 0
	v_mov_b32_e32 v134, 0
	v_mov_b32_e32 v135, 0
	v_mov_b32_e32 v136, 0
	v_mov_b32_e32 v137, 0
	v_mov_b32_e32 v138, 0
	v_mov_b32_e32 v139, 0
	v_mov_b32_e32 v140, 0
	v_mov_b32_e32 v141, 0
	v_mov_b32_e32 v142, 0
	v_mov_b32_e32 v143, 0
	v_mov_b32_e32 v144, 0
	v_mov_b32_e32 v145, 0
	v_mov_b32_e32 v146, 0
	v_mov_b32_e32 v147, 0
	v_mov_b32_e32 v148, 0
	v_mov_b32_e32 v149, 0
	v_mov_b32_e32 v150, 0
	v_mov_b32_e32 v151, 0
	v_mov_b32_e32 v152, 0
	v_mov_b32_e32 v153, 0
	v_mov_b32_e32 v154, 0
	v_mov_b32_e32 v155, 0
	v_mov_b32_e32 v156, 0
	v_mov_b32_e32 v157, 0
	v_mov_b32_e32 v158, 0
	v_mov_b32_e32 v159, 0
	v_mov_b32_e32 v160, 0
	v_mov_b32_e32 v161, 0
	v_mov_b32_e32 v162, 0
	v_mov_b32_e32 v163, 0
	v_mov_b32_e32 v164, 0
	v_mov_b32_e32 v165, 0
	v_ashrrev_i32_e32 v206, 3, v52
	v_add_u32_e32 v166, -15, v206
	v_ashrrev_i32_e32 v167, 31, v166
	v_lshl_add_u64 v[168:169], s[0:1], 0, v[166:167]
	v_mov_b64_e32 v[170:171], s[10:11]
	s_movk_i32 s98, 0x1200
	v_mad_u64_u32 v[170:171], s[100:101], v168, s98, v[170:171]
	v_mad_i32_i24 v171, v169, s98, v171
	v_and_b32_e32 v172, 7, v52
	v_lshlrev_b32_e32 v172, 4, v172
	v_mov_b32_e32 v173, 0
	v_lshl_add_u64 v[170:171], v[170:171], 0, v[172:173]
	v_add_co_u32_e32 v170, vcc, 0x1000, v170
	s_nop 1
	v_addc_co_u32_e32 v171, vcc, 0, v171, vcc
	s_mov_b64 s[100:101], 0x48000
	v_lshl_add_u64 v[174:175], v[170:171], 0, s[100:101]
	v_lshl_add_u64 v[176:177], v[174:175], 0, s[100:101]
	v_lshlrev_b32_e32 v204, 5, v52
	s_mov_b64 s[98:99], exec
	v_cmp_lt_i32_e32 vcc, s28, v166
	s_and_b64 exec, s[98:99], vcc
	global_load_dwordx4 v[118:121], v[170:171], off
	global_load_dwordx4 v[130:133], v[170:171], off offset:128
	global_load_dwordx4 v[142:145], v[170:171], off offset:256
	global_load_dwordx4 v[154:157], v[170:171], off offset:384
	s_mov_b64 exec, s[98:99]
	v_add_u32_e32 v178, 64, v166
	v_cmp_lt_i32_e32 vcc, s28, v178
	s_and_b64 exec, s[98:99], vcc
	global_load_dwordx4 v[122:125], v[174:175], off
	global_load_dwordx4 v[134:137], v[174:175], off offset:128
	global_load_dwordx4 v[146:149], v[174:175], off offset:256
	global_load_dwordx4 v[158:161], v[174:175], off offset:384
	s_mov_b64 exec, s[98:99]
	v_add_u32_e32 v178, 0x80, v166
	v_cmp_lt_i32_e32 vcc, s28, v178
	s_mov_b64 s[100:101], vcc
	v_cmp_gt_u32_e32 vcc, 0x78, v52
	s_and_b64 s[100:101], s[100:101], vcc
	s_and_b64 exec, s[98:99], s[100:101]
	global_load_dwordx4 v[126:129], v[176:177], off
	global_load_dwordx4 v[138:141], v[176:177], off offset:128
	global_load_dwordx4 v[150:153], v[176:177], off offset:256
	global_load_dwordx4 v[162:165], v[176:177], off offset:384
	s_mov_b64 exec, s[98:99]
	s_barrier
	s_waitcnt vmcnt(0)
	v_lshlrev_b32_e32 v180, 16, v118
	v_and_b32_e32 v181, 0xffff0000, v118
	v_lshlrev_b32_e32 v182, 16, v119
	v_and_b32_e32 v183, 0xffff0000, v119
	v_lshlrev_b32_e32 v184, 16, v120
	v_and_b32_e32 v185, 0xffff0000, v120
	v_lshlrev_b32_e32 v186, 16, v121
	v_and_b32_e32 v187, 0xffff0000, v121
	v_lshlrev_b32_e32 v188, 16, v122
	v_and_b32_e32 v189, 0xffff0000, v122
	v_lshlrev_b32_e32 v190, 16, v123
	v_and_b32_e32 v191, 0xffff0000, v123
	v_lshlrev_b32_e32 v192, 16, v124
	v_and_b32_e32 v193, 0xffff0000, v124
	v_lshlrev_b32_e32 v194, 16, v125
	v_and_b32_e32 v195, 0xffff0000, v125
	v_lshlrev_b32_e32 v196, 16, v126
	v_and_b32_e32 v197, 0xffff0000, v126
	v_lshlrev_b32_e32 v198, 16, v127
	v_and_b32_e32 v199, 0xffff0000, v127
	v_lshlrev_b32_e32 v200, 16, v128
	v_and_b32_e32 v201, 0xffff0000, v128
	v_lshlrev_b32_e32 v202, 16, v129
	v_and_b32_e32 v203, 0xffff0000, v129
	ds_write_b128 v204, v[180:183]
	ds_write_b128 v204, v[184:187] offset:16
	ds_write_b128 v204, v[188:191] offset:16384
	ds_write_b128 v204, v[192:195] offset:16400
	s_mov_b64 s[98:99], exec
	v_cmp_gt_u32_e32 vcc, 0x78, v52
	s_and_b64 exec, s[98:99], vcc
	ds_write_b128 v204, v[196:199] offset:32768
	ds_write_b128 v204, v[200:203] offset:32784
	s_mov_b64 exec, s[98:99]
	v_lshlrev_b32_e32 v2, 1, v40
	v_lshl_or_b32 v36, v55, 7, v2
	v_mov_b32_e32 v37, 0
	v_lshl_add_u64 v[2:3], s[14:15], 0, v[36:37]
	v_add_co_u32_e32 v4, vcc, 0x148000, v2
	s_mov_b64 s[2:3], 0x148000
	s_nop 0
	v_addc_co_u32_e32 v5, vcc, 0, v3, vcc
	v_add_co_u32_e32 v34, vcc, 0x149000, v2
	v_lshl_add_u64 v[42:43], v[2:3], 0, s[2:3]
	s_nop 0
	v_addc_co_u32_e32 v35, vcc, 0, v3, vcc
	global_load_dwordx4 v[14:17], v[42:43], off offset:64
	global_load_dwordx4 v[26:29], v[42:43], off offset:2048
	global_load_dwordx4 v[30:33], v[4:5], off
	global_load_dwordx4 v[10:13], v[42:43], off offset:2112
	global_load_dwordx4 v[22:25], v[34:35], off
	global_load_dwordx4 v[6:9], v[34:35], off offset:64
	global_load_dwordx4 v[18:21], v[34:35], off offset:2048
	s_nop 0
	global_load_dwordx4 v[2:5], v[34:35], off offset:2112
	v_lshlrev_b32_e32 v116, 4, v41
	global_load_dwordx4 v[100:103], v116, s[64:65] offset:1024
	global_load_dwordx4 v[104:107], v116, s[64:65] offset:1088
	global_load_dwordx4 v[108:111], v116, s[64:65] offset:1152
	global_load_dwordx4 v[112:115], v116, s[64:65] offset:1216
	v_add_u32_e32 v54, s12, v58
	v_add_u32_e32 v56, 1, v54
	v_cmp_gt_i32_e32 vcc, 1, v54
	v_lshlrev_b32_e32 v50, 8, v58
	v_cmp_gt_i32_e64 s[8:9], 1, v56
	v_cmp_lt_i32_e64 s[2:3], 0, v56
	v_cmp_lt_i32_e64 s[6:7], 0, v54
	v_cndmask_b32_e64 v39, 2, 1, vcc
	v_mov_b32_e32 v36, v37
	v_mov_b32_e32 v45, v37
	v_mov_b32_e32 v44, v37
	s_waitcnt lgkmcnt(0)
	s_barrier
	s_and_saveexec_b64 s[12:13], s[2:3]
	s_cbranch_execz .LBB0_990
	v_lshlrev_b32_e32 v34, 6, v1
	v_add3_u32 v34, v50, v34, 0
	v_mov_b32_e32 v44, 0
	v_add_u32_e32 v34, 0xf00, v34
	s_mov_b64 s[14:15], 0
	v_mov_b32_e32 v35, v39
	v_mov_b32_e32 v45, v44
	v_mov_b32_e32 v36, v44
	v_mov_b32_e32 v37, v44

.LBB0_1002:
	s_or_b64 exec, exec, s[12:13]
	ds_read_b128 v[46:49], v53 offset:3888
	v_mov_b32_e32 v60, v34
	v_mov_b32_e32 v61, v34
	s_movk_i32 s14, 0x7fff
	s_mov_b32 s15, 0xffff0000
	s_waitcnt lgkmcnt(0)
	v_pk_fma_f32 v[34:35], v[34:35], v[36:37], v[46:47] neg_lo:[0,0,1] neg_hi:[0,0,1]
	v_xor_b32_e32 v49, 0x80000000, v49
	v_bfe_u32 v36, v34, 16, 1
	v_xor_b32_e32 v48, 0x80000000, v48
	v_add3_u32 v34, v34, v36, s14
	v_bfe_u32 v36, v35, 16, 1
	v_pk_fma_f32 v[44:45], v[60:61], v[44:45], v[48:49]
	v_lshrrev_b32_e32 v34, 16, v34
	v_add3_u32 v35, v35, v36, s14
	v_or_b32_e32 v68, s29, v55
	s_movk_i32 s12, 0x90
	v_and_or_b32 v34, v35, s15, v34
	v_bfe_u32 v35, v44, 16, 1
	v_mul_lo_u32 v39, v68, s12
	v_add3_u32 v35, v44, v35, s14
	v_bfe_u32 v36, v45, 16, 1
	v_add_u32_e32 v39, 0, v39
	v_lshrrev_b32_e32 v35, 16, v35
	v_add3_u32 v36, v45, v36, s14
	v_and_or_b32 v35, v36, s15, v35
	v_add_u32_e32 v55, v39, v38
	ds_write_b64 v51, v[34:35] offset:40984
	s_waitcnt lgkmcnt(0)
	s_barrier
	ds_read_b128 v[34:37], v55 offset:40960
	ds_read_b128 v[44:47], v55 offset:41024
	s_waitcnt vmcnt(10) lgkmcnt(1)
	v_mfma_f32_16x16x32_bf16 v[60:63], v[26:29], v[34:37], 0
	v_lshlrev_b32_e32 v26, 4, v41
	v_ashrrev_i32_e32 v69, 31, v68
	s_waitcnt vmcnt(9)
	v_mfma_f32_16x16x32_bf16 v[30:33], v[30:33], v[34:37], 0
	s_movk_i32 s18, 0x1200
	v_mov_b64_e32 v[28:29], s[10:11]
	v_lshl_add_u64 v[38:39], s[0:1], 0, v[68:69]
	s_waitcnt lgkmcnt(0)
	v_mfma_f32_16x16x32_bf16 v[14:17], v[14:17], v[44:47], v[30:33]
	v_mad_u64_u32 v[28:29], s[12:13], v38, s18, v[28:29]
	v_mov_b32_e32 v41, 0
	v_mad_i32_i24 v29, v39, s18, v29
	v_lshl_add_u64 v[38:39], v[28:29], 0, v[40:41]
	s_waitcnt vmcnt(8)
	v_mfma_f32_16x16x32_bf16 v[10:13], v[10:13], v[44:47], v[60:63]
	s_waitcnt vmcnt(0)
	s_nop 0
	v_pk_mul_f32 v[16:17], v[16:17], v[102:103]
	v_pk_mul_f32 v[14:15], v[14:15], v[100:101]
	v_bfe_u32 v29, v16, 16, 1
	v_bfe_u32 v27, v14, 16, 1
	v_bfe_u32 v28, v15, 16, 1
	v_bfe_u32 v30, v17, 16, 1
	v_add3_u32 v14, v14, v27, s14
	v_add3_u32 v16, v16, v29, s14
	v_add3_u32 v15, v15, v28, s14
	v_add3_u32 v17, v17, v30, s14
	v_lshrrev_b32_e32 v14, 16, v14
	v_lshrrev_b32_e32 v16, 16, v16
	v_and_or_b32 v14, v15, s15, v14
	v_and_or_b32 v15, v17, s15, v16
	global_store_dwordx2 v[38:39], v[14:15], off offset:512
	v_mfma_f32_16x16x32_bf16 v[22:25], v[22:25], v[34:37], 0
	v_mov_b32_e32 v27, v41
	v_pk_mul_f32 v[12:13], v[12:13], v[106:107]
	v_pk_mul_f32 v[10:11], v[10:11], v[104:105]
	v_bfe_u32 v16, v12, 16, 1
	v_bfe_u32 v14, v10, 16, 1
	v_bfe_u32 v15, v11, 16, 1
	v_bfe_u32 v17, v13, 16, 1
	v_add3_u32 v10, v10, v14, s14
	v_add3_u32 v12, v12, v16, s14
	v_add3_u32 v11, v11, v15, s14
	v_add3_u32 v13, v13, v17, s14
	v_lshrrev_b32_e32 v10, 16, v10
	v_lshrrev_b32_e32 v12, 16, v12
	v_and_or_b32 v10, v11, s15, v10
	v_and_or_b32 v11, v13, s15, v12
	global_store_dwordx2 v[38:39], v[10:11], off offset:544
	v_mfma_f32_16x16x32_bf16 v[6:9], v[6:9], v[44:47], v[22:25]
	v_mfma_f32_16x16x32_bf16 v[18:21], v[18:21], v[34:37], 0
	v_mfma_f32_16x16x32_bf16 v[2:5], v[2:5], v[44:47], v[18:21]
	s_nop 5
	v_pk_mul_f32 v[8:9], v[8:9], v[110:111]
	v_pk_mul_f32 v[6:7], v[6:7], v[108:109]
	v_bfe_u32 v12, v8, 16, 1
	v_bfe_u32 v10, v6, 16, 1
	v_bfe_u32 v11, v7, 16, 1
	v_bfe_u32 v13, v9, 16, 1
	v_add3_u32 v6, v6, v10, s14
	v_add3_u32 v8, v8, v12, s14
	v_add3_u32 v7, v7, v11, s14
	v_add3_u32 v9, v9, v13, s14
	v_lshrrev_b32_e32 v6, 16, v6
	v_lshrrev_b32_e32 v8, 16, v8
	v_and_or_b32 v6, v7, s15, v6
	v_and_or_b32 v7, v9, s15, v8
	global_store_dwordx2 v[38:39], v[6:7], off offset:576
	v_pk_mul_f32 v[4:5], v[4:5], v[114:115]
	v_pk_mul_f32 v[2:3], v[2:3], v[112:113]
	v_bfe_u32 v8, v4, 16, 1
	v_bfe_u32 v6, v2, 16, 1
	v_bfe_u32 v7, v3, 16, 1
	v_bfe_u32 v9, v5, 16, 1
	v_add3_u32 v2, v2, v6, s14
	v_add3_u32 v4, v4, v8, s14
	v_add3_u32 v3, v3, v7, s14
	v_add3_u32 v5, v5, v9, s14
	v_lshrrev_b32_e32 v2, 16, v2
	v_lshrrev_b32_e32 v4, 16, v4
	v_and_or_b32 v2, v3, s15, v2
	v_and_or_b32 v3, v5, s15, v4
	global_store_dwordx2 v[38:39], v[2:3], off offset:608
	s_barrier
	v_lshlrev_b32_e32 v180, 16, v130
	v_and_b32_e32 v181, 0xffff0000, v130
	v_lshlrev_b32_e32 v182, 16, v131
	v_and_b32_e32 v183, 0xffff0000, v131
	v_lshlrev_b32_e32 v184, 16, v132
	v_and_b32_e32 v185, 0xffff0000, v132
	v_lshlrev_b32_e32 v186, 16, v133
	v_and_b32_e32 v187, 0xffff0000, v133
	v_lshlrev_b32_e32 v188, 16, v134
	v_and_b32_e32 v189, 0xffff0000, v134
	v_lshlrev_b32_e32 v190, 16, v135
	v_and_b32_e32 v191, 0xffff0000, v135
	v_lshlrev_b32_e32 v192, 16, v136
	v_and_b32_e32 v193, 0xffff0000, v136
	v_lshlrev_b32_e32 v194, 16, v137
	v_and_b32_e32 v195, 0xffff0000, v137
	v_lshlrev_b32_e32 v196, 16, v138
	v_and_b32_e32 v197, 0xffff0000, v138
	v_lshlrev_b32_e32 v198, 16, v139
	v_and_b32_e32 v199, 0xffff0000, v139
	v_lshlrev_b32_e32 v200, 16, v140
	v_and_b32_e32 v201, 0xffff0000, v140
	v_lshlrev_b32_e32 v202, 16, v141
	v_and_b32_e32 v203, 0xffff0000, v141
	ds_write_b128 v204, v[180:183]
	ds_write_b128 v204, v[184:187] offset:16
	ds_write_b128 v204, v[188:191] offset:16384
	ds_write_b128 v204, v[192:195] offset:16400
	s_mov_b64 s[98:99], exec
	v_cmp_gt_u32_e32 vcc, 0x78, v52
	s_and_b64 exec, s[98:99], vcc
	ds_write_b128 v204, v[196:199] offset:32768
	ds_write_b128 v204, v[200:203] offset:32784
	s_mov_b64 exec, s[98:99]
	v_add_co_u32_e32 v2, vcc, 0x2000, v42
	v_lshl_add_u64 v[40:41], s[64:65], 0, v[26:27]
	s_nop 0
	v_addc_co_u32_e32 v3, vcc, 0, v43, vcc
	v_add_co_u32_e32 v34, vcc, 0x3000, v42
	global_load_dwordx4 v[18:21], v[2:3], off
	global_load_dwordx4 v[14:17], v[2:3], off offset:64
	global_load_dwordx4 v[22:25], v[2:3], off offset:2048
	global_load_dwordx4 v[10:13], v[2:3], off offset:2112
	v_addc_co_u32_e32 v35, vcc, 0, v43, vcc
	global_load_dwordx4 v[26:29], v[34:35], off
	global_load_dwordx4 v[6:9], v[34:35], off offset:64
	global_load_dwordx4 v[30:33], v[34:35], off offset:2048
	global_load_dwordx4 v[2:5], v[34:35], off offset:2112
	global_load_dwordx4 v[100:103], v[40:41], off offset:1280
	global_load_dwordx4 v[104:107], v[40:41], off offset:1344
	global_load_dwordx4 v[108:111], v[40:41], off offset:1408
	global_load_dwordx4 v[112:115], v[40:41], off offset:1472
	v_max_i32_e32 v34, 0, v54
	v_add_u32_e32 v60, 1, v34
	v_mov_b32_e32 v45, 0
	v_min_u32_e32 v46, 4, v60
	v_mov_b32_e32 v44, v45
	v_mov_b32_e32 v37, v45
	v_mov_b32_e32 v36, v45
	s_waitcnt lgkmcnt(0)
	s_barrier
	s_and_saveexec_b64 s[12:13], s[2:3]
	s_cbranch_execz .LBB0_1011
	v_lshlrev_b32_e32 v34, 6, v1
	v_add3_u32 v34, v50, v34, 0
	v_mov_b32_e32 v36, 0
	v_add_u32_e32 v34, 0xf00, v34
	s_mov_b64 s[14:15], 0
	v_mov_b32_e32 v35, v46
	v_mov_b32_e32 v37, v36
	v_mov_b32_e32 v44, v36
	v_mov_b32_e32 v45, v36

.LBB0_1023:
	s_or_b64 exec, exec, s[12:13]
	ds_read_b128 v[46:49], v53 offset:3888
	v_mov_b32_e32 v62, v34
	v_mov_b32_e32 v63, v34
	s_movk_i32 s12, 0x7fff
	s_mov_b32 s13, 0xffff0000
	s_waitcnt lgkmcnt(0)
	v_xor_b32_e32 v49, 0x80000000, v49
	v_xor_b32_e32 v48, 0x80000000, v48
	v_pk_fma_f32 v[34:35], v[34:35], v[36:37], v[46:47] neg_lo:[0,0,1] neg_hi:[0,0,1]
	v_pk_fma_f32 v[36:37], v[62:63], v[44:45], v[48:49]
	v_bfe_u32 v44, v34, 16, 1
	v_add3_u32 v34, v34, v44, s12
	v_bfe_u32 v44, v35, 16, 1
	v_lshrrev_b32_e32 v34, 16, v34
	v_add3_u32 v35, v35, v44, s12
	v_and_or_b32 v34, v35, s13, v34
	v_bfe_u32 v35, v36, 16, 1
	v_add3_u32 v35, v36, v35, s12
	v_bfe_u32 v36, v37, 16, 1
	v_lshrrev_b32_e32 v35, 16, v35
	v_add3_u32 v36, v37, v36, s12
	v_and_or_b32 v35, v36, s13, v35
	ds_write_b64 v51, v[34:35] offset:40984
	s_waitcnt lgkmcnt(0)
	s_barrier
	ds_read_b128 v[34:37], v55 offset:40960
	ds_read_b128 v[44:47], v55 offset:41024
	s_waitcnt vmcnt(11) lgkmcnt(1)
	v_mfma_f32_16x16x32_bf16 v[18:21], v[18:21], v[34:37], 0
	s_waitcnt vmcnt(9)
	v_mfma_f32_16x16x32_bf16 v[22:25], v[22:25], v[34:37], 0
	s_waitcnt vmcnt(7)
	v_mfma_f32_16x16x32_bf16 v[26:29], v[26:29], v[34:37], 0
	s_waitcnt vmcnt(5)
	v_mfma_f32_16x16x32_bf16 v[30:33], v[30:33], v[34:37], 0
	s_waitcnt lgkmcnt(0)
	v_mfma_f32_16x16x32_bf16 v[14:17], v[14:17], v[44:47], v[18:21]
	v_mfma_f32_16x16x32_bf16 v[10:13], v[10:13], v[44:47], v[22:25]
	v_mfma_f32_16x16x32_bf16 v[6:9], v[6:9], v[44:47], v[26:29]
	s_waitcnt vmcnt(0)
	s_nop 4
	v_pk_mul_f32 v[16:17], v[16:17], v[102:103]
	v_pk_mul_f32 v[14:15], v[14:15], v[100:101]
	v_bfe_u32 v20, v16, 16, 1
	v_bfe_u32 v18, v14, 16, 1
	v_bfe_u32 v19, v15, 16, 1
	v_bfe_u32 v21, v17, 16, 1
	v_add3_u32 v14, v14, v18, s12
	v_add3_u32 v16, v16, v20, s12
	v_add3_u32 v15, v15, v19, s12
	v_add3_u32 v17, v17, v21, s12
	v_lshrrev_b32_e32 v14, 16, v14
	v_lshrrev_b32_e32 v16, 16, v16
	v_and_or_b32 v14, v15, s13, v14
	v_and_or_b32 v15, v17, s13, v16
	global_store_dwordx2 v[38:39], v[14:15], off offset:640
	v_mfma_f32_16x16x32_bf16 v[2:5], v[2:5], v[44:47], v[30:33]
	v_pk_mul_f32 v[12:13], v[12:13], v[106:107]
	v_pk_mul_f32 v[10:11], v[10:11], v[104:105]
	v_bfe_u32 v16, v12, 16, 1
	v_bfe_u32 v14, v10, 16, 1
	v_bfe_u32 v15, v11, 16, 1
	v_bfe_u32 v17, v13, 16, 1
	v_add3_u32 v10, v10, v14, s12
	v_add3_u32 v12, v12, v16, s12
	v_add3_u32 v11, v11, v15, s12
	v_add3_u32 v13, v13, v17, s12
	v_lshrrev_b32_e32 v10, 16, v10
	v_lshrrev_b32_e32 v12, 16, v12
	v_and_or_b32 v10, v11, s13, v10
	v_and_or_b32 v11, v13, s13, v12
	global_store_dwordx2 v[38:39], v[10:11], off offset:672
	v_pk_mul_f32 v[8:9], v[8:9], v[110:111]
	v_pk_mul_f32 v[6:7], v[6:7], v[108:109]
	v_bfe_u32 v12, v8, 16, 1
	v_bfe_u32 v10, v6, 16, 1
	v_bfe_u32 v11, v7, 16, 1
	v_bfe_u32 v13, v9, 16, 1
	v_add3_u32 v6, v6, v10, s12
	v_add3_u32 v8, v8, v12, s12
	v_add3_u32 v7, v7, v11, s12
	v_add3_u32 v9, v9, v13, s12
	v_lshrrev_b32_e32 v6, 16, v6
	v_lshrrev_b32_e32 v8, 16, v8
	v_and_or_b32 v6, v7, s13, v6
	v_and_or_b32 v7, v9, s13, v8
	global_store_dwordx2 v[38:39], v[6:7], off offset:704
	v_pk_mul_f32 v[4:5], v[4:5], v[114:115]
	v_pk_mul_f32 v[2:3], v[2:3], v[112:113]
	v_bfe_u32 v8, v4, 16, 1
	v_bfe_u32 v6, v2, 16, 1
	v_bfe_u32 v7, v3, 16, 1
	v_bfe_u32 v9, v5, 16, 1
	v_add3_u32 v2, v2, v6, s12
	v_add3_u32 v4, v4, v8, s12
	v_add3_u32 v3, v3, v7, s12
	v_add3_u32 v5, v5, v9, s12
	v_lshrrev_b32_e32 v2, 16, v2
	v_lshrrev_b32_e32 v4, 16, v4
	v_and_or_b32 v2, v3, s13, v2
	v_and_or_b32 v3, v5, s13, v4
	global_store_dwordx2 v[38:39], v[2:3], off offset:736
	s_barrier
	v_lshlrev_b32_e32 v180, 16, v142
	v_and_b32_e32 v181, 0xffff0000, v142
	v_lshlrev_b32_e32 v182, 16, v143
	v_and_b32_e32 v183, 0xffff0000, v143
	v_lshlrev_b32_e32 v184, 16, v144
	v_and_b32_e32 v185, 0xffff0000, v144
	v_lshlrev_b32_e32 v186, 16, v145
	v_and_b32_e32 v187, 0xffff0000, v145
	v_lshlrev_b32_e32 v188, 16, v146
	v_and_b32_e32 v189, 0xffff0000, v146
	v_lshlrev_b32_e32 v190, 16, v147
	v_and_b32_e32 v191, 0xffff0000, v147
	v_lshlrev_b32_e32 v192, 16, v148
	v_and_b32_e32 v193, 0xffff0000, v148
	v_lshlrev_b32_e32 v194, 16, v149
	v_and_b32_e32 v195, 0xffff0000, v149
	v_lshlrev_b32_e32 v196, 16, v150
	v_and_b32_e32 v197, 0xffff0000, v150
	v_lshlrev_b32_e32 v198, 16, v151
	v_and_b32_e32 v199, 0xffff0000, v151
	v_lshlrev_b32_e32 v200, 16, v152
	v_and_b32_e32 v201, 0xffff0000, v152
	v_lshlrev_b32_e32 v202, 16, v153
	v_and_b32_e32 v203, 0xffff0000, v153
	ds_write_b128 v204, v[180:183]
	ds_write_b128 v204, v[184:187] offset:16
	ds_write_b128 v204, v[188:191] offset:16384
	ds_write_b128 v204, v[192:195] offset:16400
	s_mov_b64 s[98:99], exec
	v_cmp_gt_u32_e32 vcc, 0x78, v52
	s_and_b64 exec, s[98:99], vcc
	ds_write_b128 v204, v[196:199] offset:32768
	ds_write_b128 v204, v[200:203] offset:32784
	s_mov_b64 exec, s[98:99]
	v_add_co_u32_e32 v2, vcc, 0x4000, v42
	s_nop 1
	v_addc_co_u32_e32 v3, vcc, 0, v43, vcc
	v_add_co_u32_e32 v34, vcc, 0x5000, v42
	global_load_dwordx4 v[18:21], v[2:3], off
	global_load_dwordx4 v[14:17], v[2:3], off offset:64
	global_load_dwordx4 v[22:25], v[2:3], off offset:2048
	global_load_dwordx4 v[10:13], v[2:3], off offset:2112
	v_addc_co_u32_e32 v35, vcc, 0, v43, vcc
	global_load_dwordx4 v[26:29], v[34:35], off
	global_load_dwordx4 v[6:9], v[34:35], off offset:64
	global_load_dwordx4 v[30:33], v[34:35], off offset:2048
	global_load_dwordx4 v[2:5], v[34:35], off offset:2112
	global_load_dwordx4 v[100:103], v[40:41], off offset:1536
	global_load_dwordx4 v[104:107], v[40:41], off offset:1600
	global_load_dwordx4 v[108:111], v[40:41], off offset:1664
	global_load_dwordx4 v[112:115], v[40:41], off offset:1728
	s_waitcnt lgkmcnt(0)
	s_barrier
	s_and_saveexec_b64 s[12:13], s[8:9]
	s_xor_b64 s[12:13], exec, s[12:13]
	ds_read_b128 v[34:37], v53 offset:3840
	s_or_saveexec_b64 s[12:13], s[12:13]
	v_lshl_add_u32 v59, v59, 2, 0
	v_add_u32_e32 v44, 15, v58
	v_mov_b32_e32 v46, 0
	v_lshl_add_u32 v58, v44, 8, v59
	v_mov_b32_e32 v47, 0
	v_mov_b32_e32 v48, 0
	v_mov_b32_e32 v49, 0
	s_xor_b64 exec, exec, s[12:13]
	s_cbranch_execz .LBB0_1046
	s_waitcnt lgkmcnt(0)
	ds_read_b128 v[34:37], v58
	s_waitcnt lgkmcnt(0)
	v_pk_add_f32 v[48:49], v[36:37], 0 op_sel_hi:[1,0]
	v_pk_add_f32 v[46:47], v[34:35], 0 op_sel_hi:[1,0]
	s_and_saveexec_b64 s[14:15], s[6:7]
	s_cbranch_execz .LBB0_1045
	v_add_u32_e32 v44, v59, v50
	ds_read_b128 v[62:65], v44 offset:3584
	v_cmp_ne_u32_e32 vcc, 2, v60
	s_waitcnt lgkmcnt(0)
	v_pk_add_f32 v[48:49], v[48:49], v[64:65]
	v_pk_add_f32 v[46:47], v[46:47], v[62:63]
	s_and_saveexec_b64 s[16:17], vcc
	s_cbranch_execz .LBB0_1044
	ds_read_b128 v[62:65], v44 offset:3328
	v_cmp_ne_u32_e32 vcc, 3, v60
	s_waitcnt lgkmcnt(0)
	v_pk_add_f32 v[48:49], v[48:49], v[64:65]
	v_pk_add_f32 v[46:47], v[46:47], v[62:63]
	s_and_saveexec_b64 s[18:19], vcc
	s_cbranch_execz .LBB0_1043
	ds_read_b128 v[62:65], v44 offset:3072
	v_cmp_ne_u32_e32 vcc, 4, v60
	s_waitcnt lgkmcnt(0)
	v_pk_add_f32 v[48:49], v[48:49], v[64:65]
	v_pk_add_f32 v[46:47], v[46:47], v[62:63]
	s_and_saveexec_b64 s[20:21], vcc
	s_cbranch_execz .LBB0_1042
	ds_read_b128 v[62:65], v44 offset:2816
	v_cmp_ne_u32_e32 vcc, 5, v60
	s_waitcnt lgkmcnt(0)
	v_pk_add_f32 v[48:49], v[48:49], v[64:65]
	v_pk_add_f32 v[46:47], v[46:47], v[62:63]
	s_and_saveexec_b64 s[22:23], vcc
	s_cbranch_execz .LBB0_1041
	ds_read_b128 v[62:65], v44 offset:2560
	v_cmp_ne_u32_e32 vcc, 6, v60
	s_waitcnt lgkmcnt(0)
	v_pk_add_f32 v[48:49], v[48:49], v[64:65]
	v_pk_add_f32 v[46:47], v[46:47], v[62:63]
	s_and_saveexec_b64 s[24:25], vcc
	s_cbranch_execz .LBB0_1040
	ds_read_b128 v[62:65], v44 offset:2304
	v_cmp_ne_u32_e32 vcc, 7, v60
	s_waitcnt lgkmcnt(0)
	v_pk_add_f32 v[48:49], v[48:49], v[64:65]
	v_pk_add_f32 v[46:47], v[46:47], v[62:63]
	s_and_saveexec_b64 s[26:27], vcc
	s_cbranch_execz .LBB0_1039
	ds_read_b128 v[62:65], v44 offset:2048
	s_waitcnt lgkmcnt(0)
	v_pk_add_f32 v[48:49], v[48:49], v[64:65]
	v_pk_add_f32 v[46:47], v[46:47], v[62:63]

.LBB0_1100:
	s_or_b64 exec, exec, s[8:9]
	s_waitcnt lgkmcnt(0)
	v_pk_fma_f32 v[34:35], v[44:45], v[46:47], v[34:35] neg_lo:[0,0,1] neg_hi:[0,0,1]
	v_mov_b32_e32 v58, v44
	v_mov_b32_e32 v59, v44
	v_bfe_u32 v44, v34, 16, 1
	s_movk_i32 s6, 0x7fff
	v_xor_b32_e32 v37, 0x80000000, v37
	v_xor_b32_e32 v36, 0x80000000, v36
	v_add3_u32 v34, v34, v44, s6
	v_bfe_u32 v44, v35, 16, 1
	v_pk_fma_f32 v[36:37], v[58:59], v[48:49], v[36:37]
	v_lshrrev_b32_e32 v34, 16, v34
	v_add3_u32 v35, v35, v44, s6
	s_mov_b32 s7, 0xffff0000
	v_and_or_b32 v34, v35, s7, v34
	v_bfe_u32 v35, v36, 16, 1
	v_add3_u32 v35, v36, v35, s6
	v_bfe_u32 v36, v37, 16, 1
	v_lshrrev_b32_e32 v35, 16, v35
	v_add3_u32 v36, v37, v36, s6
	v_and_or_b32 v35, v36, s7, v35
	ds_write_b64 v51, v[34:35] offset:40984
	s_waitcnt lgkmcnt(0)
	s_barrier
	ds_read_b128 v[34:37], v55 offset:40960
	ds_read_b128 v[44:47], v55 offset:41024
	s_waitcnt vmcnt(11) lgkmcnt(1)
	v_mfma_f32_16x16x32_bf16 v[18:21], v[18:21], v[34:37], 0
	s_waitcnt vmcnt(9)
	v_mfma_f32_16x16x32_bf16 v[22:25], v[22:25], v[34:37], 0
	s_waitcnt vmcnt(7)
	v_mfma_f32_16x16x32_bf16 v[26:29], v[26:29], v[34:37], 0
	s_waitcnt vmcnt(5)
	v_mfma_f32_16x16x32_bf16 v[30:33], v[30:33], v[34:37], 0
	s_waitcnt lgkmcnt(0)
	v_mfma_f32_16x16x32_bf16 v[14:17], v[14:17], v[44:47], v[18:21]
	v_mfma_f32_16x16x32_bf16 v[10:13], v[10:13], v[44:47], v[22:25]
	v_mfma_f32_16x16x32_bf16 v[6:9], v[6:9], v[44:47], v[26:29]
	s_waitcnt vmcnt(0)
	s_nop 4
	v_pk_mul_f32 v[16:17], v[16:17], v[102:103]
	v_pk_mul_f32 v[14:15], v[14:15], v[100:101]
	v_bfe_u32 v20, v16, 16, 1
	v_bfe_u32 v18, v14, 16, 1
	v_bfe_u32 v19, v15, 16, 1
	v_bfe_u32 v21, v17, 16, 1
	v_add3_u32 v14, v14, v18, s6
	v_add3_u32 v16, v16, v20, s6
	v_add3_u32 v15, v15, v19, s6
	v_add3_u32 v17, v17, v21, s6
	v_lshrrev_b32_e32 v14, 16, v14
	v_lshrrev_b32_e32 v16, 16, v16
	v_and_or_b32 v14, v15, s7, v14
	v_and_or_b32 v15, v17, s7, v16
	global_store_dwordx2 v[38:39], v[14:15], off offset:768
	v_mfma_f32_16x16x32_bf16 v[2:5], v[2:5], v[44:47], v[30:33]
	v_pk_mul_f32 v[12:13], v[12:13], v[106:107]
	v_pk_mul_f32 v[10:11], v[10:11], v[104:105]
	v_bfe_u32 v16, v12, 16, 1
	v_bfe_u32 v14, v10, 16, 1
	v_bfe_u32 v15, v11, 16, 1
	v_bfe_u32 v17, v13, 16, 1
	v_add3_u32 v10, v10, v14, s6
	v_add3_u32 v12, v12, v16, s6
	v_add3_u32 v11, v11, v15, s6
	v_add3_u32 v13, v13, v17, s6
	v_lshrrev_b32_e32 v10, 16, v10
	v_lshrrev_b32_e32 v12, 16, v12
	v_and_or_b32 v10, v11, s7, v10
	v_and_or_b32 v11, v13, s7, v12
	global_store_dwordx2 v[38:39], v[10:11], off offset:800
	v_pk_mul_f32 v[8:9], v[8:9], v[110:111]
	v_pk_mul_f32 v[6:7], v[6:7], v[108:109]
	v_bfe_u32 v12, v8, 16, 1
	v_bfe_u32 v10, v6, 16, 1
	v_bfe_u32 v11, v7, 16, 1
	v_bfe_u32 v13, v9, 16, 1
	v_add3_u32 v6, v6, v10, s6
	v_add3_u32 v8, v8, v12, s6
	v_add3_u32 v7, v7, v11, s6
	v_add3_u32 v9, v9, v13, s6
	v_lshrrev_b32_e32 v6, 16, v6
	v_lshrrev_b32_e32 v8, 16, v8
	v_and_or_b32 v6, v7, s7, v6
	v_and_or_b32 v7, v9, s7, v8
	global_store_dwordx2 v[38:39], v[6:7], off offset:832
	v_pk_mul_f32 v[4:5], v[4:5], v[114:115]
	v_pk_mul_f32 v[2:3], v[2:3], v[112:113]
	v_bfe_u32 v8, v4, 16, 1
	v_bfe_u32 v6, v2, 16, 1
	v_bfe_u32 v7, v3, 16, 1
	v_bfe_u32 v9, v5, 16, 1
	v_add3_u32 v2, v2, v6, s6
	v_add3_u32 v4, v4, v8, s6
	v_add3_u32 v3, v3, v7, s6
	v_add3_u32 v5, v5, v9, s6
	v_lshrrev_b32_e32 v2, 16, v2
	v_lshrrev_b32_e32 v4, 16, v4
	v_and_or_b32 v2, v3, s7, v2
	v_and_or_b32 v3, v5, s7, v4
	global_store_dwordx2 v[38:39], v[2:3], off offset:864
	s_barrier
	v_lshlrev_b32_e32 v180, 16, v154
	v_and_b32_e32 v181, 0xffff0000, v154
	v_lshlrev_b32_e32 v182, 16, v155
	v_and_b32_e32 v183, 0xffff0000, v155
	v_lshlrev_b32_e32 v184, 16, v156
	v_and_b32_e32 v185, 0xffff0000, v156
	v_lshlrev_b32_e32 v186, 16, v157
	v_and_b32_e32 v187, 0xffff0000, v157
	v_lshlrev_b32_e32 v188, 16, v158
	v_and_b32_e32 v189, 0xffff0000, v158
	v_lshlrev_b32_e32 v190, 16, v159
	v_and_b32_e32 v191, 0xffff0000, v159
	v_lshlrev_b32_e32 v192, 16, v160
	v_and_b32_e32 v193, 0xffff0000, v160
	v_lshlrev_b32_e32 v194, 16, v161
	v_and_b32_e32 v195, 0xffff0000, v161
	v_lshlrev_b32_e32 v196, 16, v162
	v_and_b32_e32 v197, 0xffff0000, v162
	v_lshlrev_b32_e32 v198, 16, v163
	v_and_b32_e32 v199, 0xffff0000, v163
	v_lshlrev_b32_e32 v200, 16, v164
	v_and_b32_e32 v201, 0xffff0000, v164
	v_lshlrev_b32_e32 v202, 16, v165
	v_and_b32_e32 v203, 0xffff0000, v165
	ds_write_b128 v204, v[180:183]
	ds_write_b128 v204, v[184:187] offset:16
	ds_write_b128 v204, v[188:191] offset:16384
	ds_write_b128 v204, v[192:195] offset:16400
	s_mov_b64 s[98:99], exec
	v_cmp_gt_u32_e32 vcc, 0x78, v52
	s_and_b64 exec, s[98:99], vcc
	ds_write_b128 v204, v[196:199] offset:32768
	ds_write_b128 v204, v[200:203] offset:32784
	s_mov_b64 exec, s[98:99]
	v_add_co_u32_e32 v2, vcc, 0x6000, v42
	v_min_u32_e32 v44, 16, v60
	s_nop 0
	v_addc_co_u32_e32 v3, vcc, 0, v43, vcc
	v_add_co_u32_e32 v34, vcc, 0x7000, v42
	global_load_dwordx4 v[18:21], v[2:3], off
	global_load_dwordx4 v[14:17], v[2:3], off offset:64
	global_load_dwordx4 v[22:25], v[2:3], off offset:2048
	global_load_dwordx4 v[10:13], v[2:3], off offset:2112
	v_addc_co_u32_e32 v35, vcc, 0, v43, vcc
	global_load_dwordx4 v[26:29], v[34:35], off
	global_load_dwordx4 v[6:9], v[34:35], off offset:64
	global_load_dwordx4 v[30:33], v[34:35], off offset:2048
	global_load_dwordx4 v[2:5], v[34:35], off offset:2112
	global_load_dwordx4 v[100:103], v[40:41], off offset:1792
	global_load_dwordx4 v[104:107], v[40:41], off offset:1856
	global_load_dwordx4 v[108:111], v[40:41], off offset:1920
	global_load_dwordx4 v[112:115], v[40:41], off offset:1984
	v_mov_b32_e32 v43, 0
	v_mov_b32_e32 v42, 0
	v_mov_b32_e32 v37, 0
	v_mov_b32_e32 v36, 0
	s_waitcnt lgkmcnt(0)
	s_barrier
	s_and_saveexec_b64 s[0:1], s[2:3]
	s_cbranch_execz .LBB0_1115
	v_mov_b32_e32 v36, 0
	v_cmp_lt_i32_e32 vcc, 6, v54
	s_mov_b32 s8, 0
	v_mov_b32_e32 v37, v36
	v_mov_b32_e32 v42, v36
	v_mov_b32_e32 v43, v36
	v_mov_b32_e32 v34, v36
	s_and_saveexec_b64 s[4:5], vcc
	s_cbranch_execz .LBB0_1110
	v_lshlrev_b32_e32 v35, 6, v1
	v_add3_u32 v35, v50, v35, 0
	v_mov_b32_e32 v36, 0
	v_and_b32_e32 v34, 24, v44
	v_add_u32_e32 v35, 0x800, v35
	s_mov_b64 s[6:7], 0
	v_mov_b32_e32 v37, v36
	v_mov_b32_e32 v42, v36
	v_mov_b32_e32 v43, v36

.LBB0_1145:
	s_or_b64 exec, exec, s[0:1]
	ds_read_b128 v[44:47], v53 offset:3888
	v_mov_b32_e32 v48, v34
	v_mov_b32_e32 v49, v34
	s_movk_i32 s0, 0x7fff
	s_mov_b32 s1, 0xffff0000
	s_waitcnt lgkmcnt(0)
	v_pk_fma_f32 v[34:35], v[34:35], v[36:37], v[44:45] neg_lo:[0,0,1] neg_hi:[0,0,1]
	v_xor_b32_e32 v47, 0x80000000, v47
	v_bfe_u32 v1, v34, 16, 1
	v_xor_b32_e32 v46, 0x80000000, v46
	v_add3_u32 v1, v34, v1, s0
	v_bfe_u32 v34, v35, 16, 1
	v_pk_fma_f32 v[36:37], v[48:49], v[42:43], v[46:47]
	v_lshrrev_b32_e32 v1, 16, v1
	v_add3_u32 v34, v35, v34, s0
	v_and_or_b32 v34, v34, s1, v1
	v_bfe_u32 v1, v36, 16, 1
	v_add3_u32 v1, v36, v1, s0
	v_bfe_u32 v35, v37, 16, 1
	v_lshrrev_b32_e32 v1, 16, v1
	v_add3_u32 v35, v37, v35, s0
	v_and_or_b32 v35, v35, s1, v1
	ds_write_b64 v51, v[34:35] offset:40984
	s_waitcnt lgkmcnt(0)
	s_barrier
	ds_read_b128 v[34:37], v55 offset:40960
	ds_read_b128 v[42:45], v55 offset:41024
	s_waitcnt vmcnt(11) lgkmcnt(1)
	v_mfma_f32_16x16x32_bf16 v[18:21], v[18:21], v[34:37], 0
	s_mov_b32 s3, 0
	s_waitcnt vmcnt(9)
	v_mfma_f32_16x16x32_bf16 v[22:25], v[22:25], v[34:37], 0
	s_waitcnt vmcnt(7)
	v_mfma_f32_16x16x32_bf16 v[26:29], v[26:29], v[34:37], 0
	s_waitcnt vmcnt(5)
	v_mfma_f32_16x16x32_bf16 v[30:33], v[30:33], v[34:37], 0
	s_waitcnt lgkmcnt(0)
	v_mfma_f32_16x16x32_bf16 v[14:17], v[14:17], v[42:45], v[18:21]
	v_mfma_f32_16x16x32_bf16 v[10:13], v[10:13], v[42:45], v[22:25]
	v_mfma_f32_16x16x32_bf16 v[6:9], v[6:9], v[42:45], v[26:29]
	s_waitcnt vmcnt(0)
	s_nop 4
	v_pk_mul_f32 v[16:17], v[16:17], v[102:103]
	v_pk_mul_f32 v[14:15], v[14:15], v[100:101]
	v_bfe_u32 v19, v16, 16, 1
	v_bfe_u32 v1, v14, 16, 1
	v_bfe_u32 v18, v15, 16, 1
	v_bfe_u32 v20, v17, 16, 1
	v_add3_u32 v1, v14, v1, s0
	v_add3_u32 v14, v15, v18, s0
	v_add3_u32 v15, v16, v19, s0
	v_add3_u32 v16, v17, v20, s0
	v_lshrrev_b32_e32 v1, 16, v1
	v_lshrrev_b32_e32 v15, 16, v15
	v_and_or_b32 v14, v14, s1, v1
	v_and_or_b32 v15, v16, s1, v15
	global_store_dwordx2 v[38:39], v[14:15], off offset:896
	v_mfma_f32_16x16x32_bf16 v[2:5], v[2:5], v[42:45], v[30:33]
	v_pk_mul_f32 v[12:13], v[12:13], v[106:107]
	v_pk_mul_f32 v[10:11], v[10:11], v[104:105]
	v_bfe_u32 v15, v12, 16, 1
	v_bfe_u32 v1, v10, 16, 1
	v_bfe_u32 v14, v11, 16, 1
	v_bfe_u32 v16, v13, 16, 1
	v_add3_u32 v1, v10, v1, s0
	v_add3_u32 v10, v11, v14, s0
	v_add3_u32 v11, v12, v15, s0
	v_add3_u32 v12, v13, v16, s0
	v_lshrrev_b32_e32 v1, 16, v1
	v_lshrrev_b32_e32 v11, 16, v11
	v_and_or_b32 v10, v10, s1, v1
	v_and_or_b32 v11, v12, s1, v11
	global_store_dwordx2 v[38:39], v[10:11], off offset:928
	v_pk_mul_f32 v[8:9], v[8:9], v[110:111]
	v_pk_mul_f32 v[6:7], v[6:7], v[108:109]
	v_bfe_u32 v11, v8, 16, 1
	v_bfe_u32 v1, v6, 16, 1
	v_bfe_u32 v10, v7, 16, 1
	v_bfe_u32 v12, v9, 16, 1
	v_add3_u32 v1, v6, v1, s0
	v_add3_u32 v6, v7, v10, s0
	v_add3_u32 v7, v8, v11, s0
	v_add3_u32 v8, v9, v12, s0
	v_lshrrev_b32_e32 v1, 16, v1
	v_lshrrev_b32_e32 v7, 16, v7
	v_and_or_b32 v6, v6, s1, v1
	v_and_or_b32 v7, v8, s1, v7
	global_store_dwordx2 v[38:39], v[6:7], off offset:960
	v_pk_mul_f32 v[4:5], v[4:5], v[114:115]
	v_pk_mul_f32 v[2:3], v[2:3], v[112:113]
	v_bfe_u32 v7, v4, 16, 1
	v_bfe_u32 v1, v2, 16, 1
	v_bfe_u32 v6, v3, 16, 1
	v_bfe_u32 v8, v5, 16, 1
	v_add3_u32 v1, v2, v1, s0
	v_add3_u32 v2, v3, v6, s0
	v_add3_u32 v3, v4, v7, s0
	v_add3_u32 v4, v5, v8, s0
	v_lshrrev_b32_e32 v1, 16, v1
	v_lshrrev_b32_e32 v3, 16, v3
	v_and_or_b32 v2, v2, s1, v1
	v_and_or_b32 v3, v4, s1, v3
	global_store_dwordx2 v[38:39], v[2:3], off offset:992
	s_barrier
	s_waitcnt vmcnt(0)
	s_barrier
	s_mov_b64 s[0:1], exec
	v_readlane_b32 s4, v254, 2
	v_readlane_b32 s5, v254, 3
	s_and_b64 s[4:5], s[0:1], s[4:5]
	s_mov_b64 exec, s[4:5]
	s_cbranch_execz .LBB0_1197
	s_mov_b32 s2, 0
	s_lshl_b64 s[2:3], s[2:3], 2
	v_readlane_b32 s4, v254, 0
	v_readlane_b32 s5, v254, 1
	s_add_u32 s2, s4, s2
	s_addc_u32 s3, s5, s3
	s_add_i32 s4, 0, 0x20160
	v_mov_b32_e32 v1, s4
	s_waitcnt vmcnt(0) expcnt(0) lgkmcnt(0)
	ds_read_b32 v3, v1
	s_add_i32 s4, 0, 0x20164
	v_mov_b32_e32 v1, s4
	ds_read_b32 v1, v1
	s_waitcnt lgkmcnt(1)
	v_cmp_ne_u32_e32 vcc, 0, v3
	s_cbranch_vccnz .LBB0_1161
	v_readlane_b32 s8, v254, 20
	v_readlane_b32 s9, v254, 21
	s_load_dword s6, s[8:9], 0x14
	s_load_dwordx2 s[4:5], s[8:9], 0x4
	s_mov_b32 s19, 1
	v_mov_b32_e32 v17, 0
	s_waitcnt lgkmcnt(0)
	s_lshr_b32 s8, s6, 16
	s_and_b32 s6, s6, 0xffff
	s_cmp_lg_u32 s6, 0
	s_cselect_b64 s[6:7], -1, 0
	s_cmp_lg_u64 s[6:7], 0
	s_addc_u32 s4, s4, 0
	v_readlane_b32 s6, v254, 22
	s_cmp_lg_u32 s8, 0
	s_mul_i32 s18, s4, s6
	s_cselect_b64 s[6:7], -1, 0
	s_cmp_lg_u64 s[6:7], 0
	s_addc_u32 s4, s5, 0
	s_mul_i32 s18, s18, s4
	s_add_u32 s4, s2, 0x1000
	s_addc_u32 s5, s3, 0
	s_add_u32 s6, s2, 0x1100
	s_addc_u32 s7, s3, 0
	s_add_u32 s8, s2, 0x1200
	s_addc_u32 s9, s3, 0
	s_add_u32 s10, s2, 0x1300
	s_addc_u32 s11, s3, 0
	s_branch .LBB0_1149

.LBB0_1233:
	s_waitcnt vmcnt(5)
	v_lshlrev_b32_e32 v217, 16, v163
	s_waitcnt lgkmcnt(2)
	v_lshlrev_b32_e32 v216, 16, v162
	v_and_b32_e32 v187, 0xffff0000, v163
	v_and_b32_e32 v186, 0xffff0000, v162
	v_pk_add_f32 v[188:189], v[216:217], v[186:187]
	v_lshlrev_b32_e32 v235, 16, v165
	v_add_f32_e32 v188, v188, v189
	v_add_f32_e32 v233, 0, v188
	v_lshlrev_b32_e32 v234, 16, v164
	v_and_b32_e32 v189, 0xffff0000, v165
	v_and_b32_e32 v188, 0xffff0000, v164
	v_pk_add_f32 v[190:191], v[234:235], v[188:189]
	s_waitcnt vmcnt(4)
	v_lshlrev_b32_e32 v194, 16, v166
	v_and_b32_e32 v195, 0xffff0000, v166
	v_lshlrev_b32_e32 v196, 16, v167
	v_and_b32_e32 v197, 0xffff0000, v167
	v_pk_add_f32 v[190:191], v[190:191], v[190:191] op_sel_hi:[0,1]
	v_lshlrev_b32_e32 v212, 16, v168
	v_and_b32_e32 v214, 0xffff0000, v168
	s_waitcnt lgkmcnt(1)
	v_lshlrev_b32_e32 v218, 16, v169
	s_waitcnt lgkmcnt(0)
	v_and_b32_e32 v232, 0xffff0000, v169
	v_add_f32_e32 v213, v194, v195
	v_add_f32_e32 v215, v196, v197
	v_mov_b32_e32 v219, v191
	v_pk_add_f32 v[192:193], v[212:213], v[214:215]
	v_pk_add_f32 v[190:191], v[218:219], v[232:233]
	s_nop 0
	v_pk_add_f32 v[190:191], v[192:193], v[190:191]
	s_nop 0
	v_add_f32_e32 v190, v190, v191
	s_waitcnt lgkmcnt(0)
	s_nop 1
	v_add_f32_dpp v190, v190, v190 quad_perm:[1,0,3,2] row_mask:0xf bank_mask:0xf
	s_nop 1
	v_add_f32_dpp v190, v190, v190 quad_perm:[2,3,0,1] row_mask:0xf bank_mask:0xf
	s_nop 1
	v_add_f32_dpp v190, v190, v190 row_half_mirror row_mask:0xf bank_mask:0xf
	s_nop 1
	v_add_f32_dpp v190, v190, v190 row_mirror row_mask:0xf bank_mask:0xf
	v_mov_b32_e32 v191, v190
	s_nop 1
	v_permlane16_swap_b32_e32 v190, v191
	v_add_f32_e32 v190, v190, v191
	v_mov_b32_e32 v191, v190
	s_nop 1
	v_permlane32_swap_b32_e32 v190, v191
	v_add_f32_e32 v210, v190, v191
	v_fmac_f32_e32 v186, 0xba800000, v210
	v_fmac_f32_e32 v187, 0xba800000, v210
	v_fmac_f32_e32 v217, 0xba800000, v210
	v_fmac_f32_e32 v216, 0xba800000, v210
	v_mov_b32_e32 v236, v217
	v_mov_b32_e32 v237, v187
	v_mov_b32_e32 v217, v186
	v_pk_mul_f32 v[190:191], v[236:237], v[236:237]
	v_pk_mul_f32 v[186:187], v[216:217], v[216:217]
	v_fmac_f32_e32 v188, 0xba800000, v210
	v_pk_mov_b32 v[192:193], v[186:187], v[190:191] op_sel:[1,0]
	v_mov_b32_e32 v187, v191
	v_fmac_f32_e32 v189, 0xba800000, v210
	v_fmac_f32_e32 v235, 0xba800000, v210
	v_pk_add_f32 v[186:187], v[192:193], v[186:187]
	v_fmac_f32_e32 v234, 0xba800000, v210
	v_mov_b32_e32 v238, v235
	v_mov_b32_e32 v239, v189
	v_mov_b32_e32 v235, v188
	v_pk_add_f32 v[186:187], v[186:187], v[186:187] op_sel_hi:[0,1]
	v_pk_mul_f32 v[190:191], v[238:239], v[238:239]
	v_pk_mul_f32 v[188:189], v[234:235], v[234:235]
	v_fmac_f32_e32 v194, 0xba800000, v210
	v_pk_mov_b32 v[192:193], v[188:189], v[190:191] op_sel:[1,0]
	v_mov_b32_e32 v189, v191
	v_fmac_f32_e32 v195, 0xba800000, v210
	v_fmac_f32_e32 v196, 0xba800000, v210
	v_mul_f32_e32 v186, v194, v194
	v_pk_add_f32 v[188:189], v[192:193], v[188:189]
	v_fmac_f32_e32 v197, 0xba800000, v210
	v_pk_fma_f32 v[190:191], v[194:195], v[194:195], v[186:187] op_sel_hi:[1,1,0]
	v_mul_f32_e32 v186, v196, v196
	v_pk_add_f32 v[188:189], v[188:189], v[188:189] op_sel_hi:[0,1]
	v_pk_fma_f32 v[192:193], v[196:197], v[196:197], v[186:187] op_sel_hi:[1,1,0]
	v_fmac_f32_e32 v232, 0xba800000, v210
	v_fmac_f32_e32 v218, 0xba800000, v210
	v_fmac_f32_e32 v214, 0xba800000, v210
	v_fmac_f32_e32 v212, 0xba800000, v210
	v_mul_f32_e32 v190, v212, v212
	v_mul_f32_e32 v192, v214, v214
	v_mul_f32_e32 v186, v218, v218
	v_mul_f32_e32 v188, v232, v232
	v_pk_add_f32 v[190:191], v[190:191], v[192:193]
	v_pk_add_f32 v[186:187], v[186:187], v[188:189]
	v_lshl_add_u64 v[210:211], s[94:95], 0, v[208:209]
	v_pk_add_f32 v[186:187], v[190:191], v[186:187]
	v_add_co_u32_e32 v190, vcc, 0xca01000, v210
	v_add_f32_e32 v186, v186, v187
	s_waitcnt lgkmcnt(0)
	v_addc_co_u32_e32 v191, vcc, 0, v211, vcc
	s_nop 1
	v_add_f32_dpp v186, v186, v186 quad_perm:[1,0,3,2] row_mask:0xf bank_mask:0xf
	s_nop 1
	v_add_f32_dpp v186, v186, v186 quad_perm:[2,3,0,1] row_mask:0xf bank_mask:0xf
	s_nop 1
	v_add_f32_dpp v186, v186, v186 row_half_mirror row_mask:0xf bank_mask:0xf
	s_nop 1
	v_add_f32_dpp v186, v186, v186 row_mirror row_mask:0xf bank_mask:0xf
	v_mov_b32_e32 v187, v186
	s_nop 1
	v_permlane16_swap_b32_e32 v186, v187
	v_add_f32_e32 v186, v186, v187
	v_mov_b32_e32 v187, v186
	s_nop 1
	v_permlane32_swap_b32_e32 v186, v187
	v_add_f32_e32 v186, v186, v187
	v_fmamk_f32 v186, v186, 0x3a800000, v228
	v_mul_f32_e32 v187, 0x4f800000, v186
	v_cmp_gt_f32_e64 s[0:1], s30, v186
	s_nop 1
	v_cndmask_b32_e64 v186, v186, v187, s[0:1]
	v_sqrt_f32_e32 v187, v186
	s_nop 0
	v_add_u32_e32 v188, -1, v187
	v_fma_f32 v189, -v188, v187, v186
	v_cmp_ge_f32_e64 s[4:5], 0, v189
	v_add_u32_e32 v189, 1, v187
	s_nop 0
	v_cndmask_b32_e64 v188, v187, v188, s[4:5]
	v_fma_f32 v187, -v189, v187, v186
	v_cmp_lt_f32_e64 s[4:5], 0, v187
	s_nop 1
	v_cndmask_b32_e64 v187, v188, v189, s[4:5]
	v_mul_f32_e32 v188, 0x37800000, v187
	v_cndmask_b32_e64 v187, v187, v188, s[0:1]
	v_cmp_class_f32_e64 s[0:1], v186, v229
	s_nop 1
	v_cndmask_b32_e64 v213, v187, v186, s[0:1]
	v_div_scale_f32 v215, s[0:1], v213, v213, 1.0
	v_rcp_f32_e32 v219, v215
	global_load_dwordx4 v[186:189], v[190:191], off offset:2048
	s_nop 0
	global_load_dwordx4 v[190:193], v[190:191], off offset:3072
	v_fma_f32 v233, -v215, v219, 1.0
	v_fmac_f32_e32 v219, v233, v219
	v_div_scale_f32 v233, vcc, 1.0, v213, 1.0
	v_mul_f32_e32 v240, v233, v219
	v_fma_f32 v241, -v215, v240, v233
	v_fmac_f32_e32 v240, v241, v219
	v_fma_f32 v215, -v215, v240, v233
	v_div_fmas_f32 v215, v215, v219, v240
	v_div_fixup_f32 v240, v215, v213, 1.0
	v_pk_mul_f32 v[216:217], v[216:217], v[240:241] op_sel_hi:[1,0]
	v_pk_mul_f32 v[194:195], v[194:195], v[240:241] op_sel_hi:[1,0]
	v_mov_b32_e32 v213, v214
	v_pk_fma_f32 v[242:243], v[2:3], v[216:217], v[6:7]
	v_pk_mul_f32 v[216:217], v[234:235], v[240:241] op_sel_hi:[1,0]
	v_pk_mul_f32 v[196:197], v[196:197], v[240:241] op_sel_hi:[1,0]
	v_pk_fma_f32 v[244:245], v[18:19], v[194:195], v[30:31]
	v_pk_mul_f32 v[194:195], v[212:213], v[240:241] op_sel_hi:[1,0]
	v_mov_b32_e32 v219, v232
	v_pk_mul_f32 v[234:235], v[238:239], v[240:241] op_sel_hi:[1,0]
	v_pk_fma_f32 v[238:239], v[14:15], v[216:217], v[26:27]
	v_pk_fma_f32 v[216:217], v[20:21], v[196:197], v[32:33]
	v_pk_mul_f32 v[196:197], v[218:219], v[240:241] op_sel_hi:[1,0]
	v_pk_fma_f32 v[218:219], v[10:11], v[194:195], v[22:23]
	v_bfe_u32 v194, v242, 16, 1
	v_pk_mul_f32 v[236:237], v[236:237], v[240:241] op_sel_hi:[1,0]
	v_add3_u32 v194, v242, v194, s31
	v_bfe_u32 v195, v243, 16, 1
	v_pk_fma_f32 v[236:237], v[4:5], v[236:237], v[8:9]
	v_lshrrev_b32_e32 v194, 16, v194
	v_add3_u32 v195, v243, v195, s31
	v_and_or_b32 v194, v195, s29, v194
	v_bfe_u32 v195, v236, 16, 1
	v_pk_fma_f32 v[214:215], v[12:13], v[196:197], v[24:25]
	v_add3_u32 v195, v236, v195, s31
	v_bfe_u32 v196, v237, 16, 1
	v_lshrrev_b32_e32 v195, 16, v195
	v_add3_u32 v196, v237, v196, s31
	v_and_or_b32 v195, v196, s29, v195
	v_bfe_u32 v196, v238, 16, 1
	v_add3_u32 v196, v238, v196, s31
	v_bfe_u32 v197, v239, 16, 1
	v_fma_f32 v240, v36, v242, 0
	v_fma_f32 v241, v37, v242, 0
	v_fma_f32 v246, v38, v242, 0
	v_fma_f32 v247, v39, v242, 0
	v_fma_f32 v248, v40, v242, 0
	v_fma_f32 v249, v41, v242, 0
	v_pk_fma_f32 v[232:233], v[34:35], v[242:243], 0 op_sel_hi:[1,0,0]
	v_pk_fma_f32 v[234:235], v[16:17], v[234:235], v[28:29]
	v_lshrrev_b32_e32 v196, 16, v196
	v_add3_u32 v197, v239, v197, s31
	v_fmac_f32_e32 v240, v44, v243
	v_fmac_f32_e32 v241, v45, v243
	v_fmac_f32_e32 v246, v46, v243
	v_fmac_f32_e32 v247, v47, v243
	v_fmac_f32_e32 v248, v48, v243
	v_fmac_f32_e32 v249, v49, v243
	v_pk_fma_f32 v[232:233], v[42:43], v[242:243], v[232:233] op_sel:[0,1,0]
	v_and_or_b32 v196, v197, s29, v196
	v_bfe_u32 v197, v234, 16, 1
	v_fmac_f32_e32 v240, v52, v236
	v_fmac_f32_e32 v241, v53, v236
	v_fmac_f32_e32 v246, v54, v236
	v_fmac_f32_e32 v247, v55, v236
	v_fmac_f32_e32 v248, v56, v236
	v_fmac_f32_e32 v249, v57, v236
	v_pk_fma_f32 v[232:233], v[50:51], v[236:237], v[232:233] op_sel_hi:[1,0,1]
	v_add3_u32 v197, v234, v197, s31
	v_bfe_u32 v212, v235, 16, 1
	v_fmac_f32_e32 v240, v60, v237
	v_fmac_f32_e32 v241, v61, v237
	v_fmac_f32_e32 v246, v62, v237
	v_fmac_f32_e32 v247, v63, v237
	v_fmac_f32_e32 v248, v64, v237
	v_fmac_f32_e32 v249, v65, v237
	v_pk_fma_f32 v[232:233], v[58:59], v[236:237], v[232:233] op_sel:[0,1,0]
	v_lshrrev_b32_e32 v197, 16, v197
	v_add3_u32 v212, v235, v212, s31
	v_fmac_f32_e32 v240, v68, v238
	v_fmac_f32_e32 v241, v69, v238
	v_fmac_f32_e32 v246, v70, v238
	v_fmac_f32_e32 v247, v71, v238
	v_fmac_f32_e32 v248, v72, v238
	v_fmac_f32_e32 v249, v73, v238
	v_pk_fma_f32 v[232:233], v[66:67], v[238:239], v[232:233] op_sel_hi:[1,0,1]
	v_and_or_b32 v197, v212, s29, v197
	v_add_co_u32_e32 v212, vcc, s33, v210
	v_fmac_f32_e32 v240, v76, v239
	v_fmac_f32_e32 v241, v77, v239
	v_fmac_f32_e32 v246, v78, v239
	v_fmac_f32_e32 v247, v79, v239
	v_fmac_f32_e32 v248, v80, v239
	v_fmac_f32_e32 v249, v81, v239
	v_pk_fma_f32 v[232:233], v[74:75], v[238:239], v[232:233] op_sel:[0,1,0]
	v_addc_co_u32_e32 v213, vcc, 0, v211, vcc
	v_fmac_f32_e32 v240, v84, v234
	v_fmac_f32_e32 v241, v85, v234
	v_fmac_f32_e32 v246, v86, v234
	v_fmac_f32_e32 v247, v87, v234
	v_fmac_f32_e32 v248, v88, v234
	v_fmac_f32_e32 v249, v89, v234
	v_pk_fma_f32 v[232:233], v[82:83], v[234:235], v[232:233] op_sel_hi:[1,0,1]
	global_store_dwordx4 v[212:213], v[194:197], off
	v_fmac_f32_e32 v240, v92, v235
	v_fmac_f32_e32 v241, v93, v235
	v_bfe_u32 v194, v244, 16, 1
	v_fmac_f32_e32 v246, v94, v235
	v_fmac_f32_e32 v247, v95, v235
	v_fmac_f32_e32 v248, v96, v235
	v_fmac_f32_e32 v249, v97, v235
	v_pk_fma_f32 v[232:233], v[90:91], v[234:235], v[232:233] op_sel:[0,1,0]
	v_add3_u32 v194, v244, v194, s31
	v_bfe_u32 v195, v245, 16, 1
	v_fmac_f32_e32 v240, v108, v244
	v_fmac_f32_e32 v241, v109, v244
	v_fmac_f32_e32 v246, v98, v244
	v_fmac_f32_e32 v247, v99, v244
	v_fmac_f32_e32 v248, v100, v244
	v_fmac_f32_e32 v249, v101, v244
	v_pk_fma_f32 v[232:233], v[106:107], v[244:245], v[232:233] op_sel_hi:[1,0,1]
	v_lshrrev_b32_e32 v194, 16, v194
	v_add3_u32 v195, v245, v195, s31
	v_pk_fma_f32 v[232:233], v[102:103], v[244:245], v[232:233] op_sel:[0,1,0]
	v_fmac_f32_e32 v240, v104, v245
	v_fmac_f32_e32 v241, v105, v245
	v_fmac_f32_e32 v246, v110, v245
	v_fmac_f32_e32 v247, v111, v245
	v_fmac_f32_e32 v248, v112, v245
	v_fmac_f32_e32 v249, v113, v245
	v_and_or_b32 v194, v195, s29, v194
	v_bfe_u32 v195, v216, 16, 1
	v_bfe_u32 v196, v217, 16, 1
	v_fmac_f32_e32 v240, v124, v216
	v_fmac_f32_e32 v241, v125, v216
	v_fmac_f32_e32 v246, v138, v216
	v_fmac_f32_e32 v247, v139, v216
	v_fmac_f32_e32 v248, v140, v216
	v_fmac_f32_e32 v249, v141, v216
	v_pk_fma_f32 v[232:233], v[122:123], v[216:217], v[232:233] op_sel_hi:[1,0,1]
	v_add3_u32 v195, v216, v195, s31
	v_add3_u32 v196, v217, v196, s31
	v_fmac_f32_e32 v240, v116, v217
	v_fmac_f32_e32 v241, v117, v217
	v_fmac_f32_e32 v246, v118, v217
	v_fmac_f32_e32 v247, v119, v217
	v_fmac_f32_e32 v248, v120, v217
	v_fmac_f32_e32 v249, v121, v217
	v_pk_fma_f32 v[216:217], v[114:115], v[216:217], v[232:233] op_sel:[0,1,0]
	v_lshrrev_b32_e32 v195, 16, v195
	v_pk_fma_f32 v[216:217], v[126:127], v[218:219], v[216:217] op_sel_hi:[1,0,1]
	v_and_or_b32 v195, v196, s29, v195
	v_pk_fma_f32 v[216:217], v[134:135], v[218:219], v[216:217] op_sel:[0,1,0]
	v_bfe_u32 v196, v218, 16, 1
	v_pk_fma_f32 v[216:217], v[142:143], v[214:215], v[216:217] op_sel_hi:[1,0,1]
	v_bfe_u32 v197, v219, 16, 1
	v_pk_fma_f32 v[216:217], v[154:155], v[214:215], v[216:217] op_sel:[0,1,0]
	ds_bpermute_b32 v232, v220, v216
	ds_bpermute_b32 v233, v220, v217
	v_fmac_f32_e32 v240, v128, v218
	v_fmac_f32_e32 v241, v129, v218
	v_fmac_f32_e32 v246, v130, v218
	v_fmac_f32_e32 v247, v131, v218
	v_fmac_f32_e32 v248, v132, v218
	v_fmac_f32_e32 v249, v133, v218
	s_waitcnt lgkmcnt(0)
	v_pk_add_f32 v[216:217], v[216:217], v[232:233]
	v_add3_u32 v196, v218, v196, s31
	v_add3_u32 v197, v219, v197, s31
	v_fmac_f32_e32 v240, v136, v219
	v_fmac_f32_e32 v241, v137, v219
	v_fmac_f32_e32 v246, v146, v219
	v_fmac_f32_e32 v247, v147, v219
	v_fmac_f32_e32 v248, v148, v219
	v_fmac_f32_e32 v249, v149, v219
	ds_bpermute_b32 v218, v221, v216
	ds_bpermute_b32 v219, v221, v217
	v_lshrrev_b32_e32 v196, 16, v196
	v_fmac_f32_e32 v240, v144, v214
	v_and_or_b32 v196, v197, s29, v196
	v_bfe_u32 v197, v214, 16, 1
	s_waitcnt lgkmcnt(0)
	v_pk_add_f32 v[216:217], v[216:217], v[218:219]
	v_fmac_f32_e32 v240, v156, v215
	v_add3_u32 v197, v214, v197, s31
	v_fmac_f32_e32 v241, v145, v214
	v_fmac_f32_e32 v246, v150, v214
	v_fmac_f32_e32 v247, v151, v214
	v_fmac_f32_e32 v248, v152, v214
	v_fmac_f32_e32 v249, v153, v214
	ds_bpermute_b32 v218, v222, v216
	ds_bpermute_b32 v219, v222, v217
	ds_bpermute_b32 v214, v220, v240
	v_fmac_f32_e32 v241, v157, v215
	v_fmac_f32_e32 v246, v158, v215
	ds_bpermute_b32 v233, v220, v241
	s_waitcnt lgkmcnt(2)
	v_pk_add_f32 v[216:217], v[216:217], v[218:219]
	s_waitcnt lgkmcnt(1)
	v_add_f32_e32 v214, v240, v214
	ds_bpermute_b32 v218, v223, v216
	ds_bpermute_b32 v219, v223, v217
	ds_bpermute_b32 v232, v221, v214
	ds_bpermute_b32 v234, v220, v246
	v_fmac_f32_e32 v247, v159, v215
	v_fmac_f32_e32 v248, v160, v215
	s_waitcnt lgkmcnt(2)
	v_pk_add_f32 v[216:217], v[216:217], v[218:219]
	s_waitcnt lgkmcnt(1)
	v_add_f32_e32 v214, v214, v232
	ds_bpermute_b32 v218, v224, v216
	ds_bpermute_b32 v219, v224, v217
	ds_bpermute_b32 v232, v222, v214
	v_fmac_f32_e32 v249, v161, v215
	ds_bpermute_b32 v238, v220, v247
	ds_bpermute_b32 v239, v220, v249
	s_waitcnt lgkmcnt(3)
	v_pk_add_f32 v[216:217], v[216:217], v[218:219]
	v_add_f32_e32 v218, v241, v233
	s_waitcnt lgkmcnt(2)
	v_add_f32_e32 v214, v214, v232
	v_add_f32_e32 v232, v246, v234
	ds_bpermute_b32 v219, v221, v218
	ds_bpermute_b32 v233, v221, v232
	ds_bpermute_b32 v234, v223, v214
	s_waitcnt lgkmcnt(4)
	v_add_f32_e32 v238, v247, v238
	s_waitcnt lgkmcnt(3)
	v_add_f32_e32 v239, v249, v239
	s_waitcnt lgkmcnt(2)
	v_add_f32_e32 v219, v218, v219
	s_waitcnt lgkmcnt(1)
	v_add_f32_e32 v232, v232, v233
	ds_bpermute_b32 v235, v222, v219
	ds_bpermute_b32 v233, v222, v232
	s_waitcnt lgkmcnt(2)
	v_add_f32_e32 v214, v214, v234
	ds_bpermute_b32 v236, v224, v214
	ds_bpermute_b32 v240, v221, v238
	s_waitcnt lgkmcnt(3)
	v_add_f32_e32 v234, v219, v235
	s_waitcnt lgkmcnt(2)
	v_add_f32_e32 v232, v232, v233
	ds_bpermute_b32 v235, v223, v234
	ds_bpermute_b32 v233, v223, v232
	s_waitcnt lgkmcnt(3)
	v_add_f32_e32 v214, v214, v236
	ds_bpermute_b32 v242, v221, v239
	s_waitcnt lgkmcnt(3)
	v_add_f32_e32 v238, v238, v240
	s_waitcnt lgkmcnt(2)
	v_add_f32_e32 v234, v234, v235
	s_waitcnt lgkmcnt(1)
	v_add_f32_e32 v236, v232, v233
	ds_bpermute_b32 v235, v224, v234
	ds_bpermute_b32 v237, v224, v236
	s_waitcnt lgkmcnt(2)
	v_add_f32_e32 v239, v239, v242
	ds_bpermute_b32 v240, v222, v238
	ds_bpermute_b32 v242, v222, v239
	s_waitcnt lgkmcnt(3)
	v_add_f32_e32 v233, v234, v235
	s_waitcnt lgkmcnt(2)
	v_add_f32_e32 v235, v236, v237
	ds_bpermute_b32 v237, v220, v248
	s_waitcnt lgkmcnt(2)
	v_add_f32_e32 v238, v238, v240
	s_waitcnt lgkmcnt(1)
	v_add_f32_e32 v239, v239, v242
	ds_bpermute_b32 v240, v223, v238
	ds_bpermute_b32 v242, v223, v239
	s_waitcnt lgkmcnt(2)
	v_add_f32_e32 v237, v248, v237
	ds_bpermute_b32 v241, v221, v237
	ds_bpermute_b32 v218, v225, v216
	s_waitcnt lgkmcnt(3)
	v_add_f32_e32 v238, v238, v240
	s_waitcnt lgkmcnt(2)
	v_add_f32_e32 v242, v239, v242
	ds_bpermute_b32 v240, v224, v238
	s_waitcnt lgkmcnt(2)
	v_add_f32_e32 v237, v237, v241
	ds_bpermute_b32 v241, v222, v237
	ds_bpermute_b32 v244, v224, v242
	ds_bpermute_b32 v219, v225, v217
	ds_bpermute_b32 v232, v225, v214
	ds_bpermute_b32 v234, v225, v233
	s_waitcnt lgkmcnt(4)
	v_add_f32_e32 v237, v237, v241
	ds_bpermute_b32 v241, v223, v237
	ds_bpermute_b32 v236, v225, v235
	v_lshrrev_b32_e32 v197, 16, v197
	s_waitcnt lgkmcnt(1)
	v_add_f32_e32 v241, v237, v241
	ds_bpermute_b32 v243, v224, v241
	v_add_f32_e32 v237, v238, v240
	ds_bpermute_b32 v238, v225, v237
	s_waitcnt lgkmcnt(1)
	v_add_f32_e32 v239, v241, v243
	v_add_f32_e32 v241, v242, v244
	ds_bpermute_b32 v240, v225, v239
	ds_bpermute_b32 v242, v225, v241
	v_bfe_u32 v243, v215, 16, 1
	v_add3_u32 v215, v215, v243, s31
	v_and_or_b32 v197, v215, s29, v197
	global_store_dwordx4 v[212:213], v[194:197], off offset:1024
	s_and_saveexec_b64 s[24:25], s[2:3]
	s_cbranch_execz .LBB0_1235
	v_pk_add_f32 v[196:197], v[216:217], v[218:219]
	v_add_f32_e32 v214, v214, v232
	v_cmp_gt_f32_e32 vcc, v197, v196
	v_add_f32_e32 v233, v233, v234
	v_add_f32_e32 v235, v235, v236
	v_cndmask_b32_e32 v194, v196, v197, vcc
	v_cmp_gt_f32_e64 s[0:1], v214, v194
	s_waitcnt lgkmcnt(2)
	v_add_f32_e32 v237, v237, v238
	s_waitcnt lgkmcnt(1)
	v_add_f32_e32 v215, v239, v240
	v_cndmask_b32_e64 v194, v194, v214, s[0:1]
	v_cmp_gt_f32_e64 s[4:5], v233, v194
	s_waitcnt lgkmcnt(0)
	v_add_f32_e32 v195, v241, v242
	v_cmp_nlg_f32_e64 s[14:15], s34, v196
	v_cndmask_b32_e64 v194, v194, v233, s[4:5]
	v_cmp_gt_f32_e64 s[6:7], v235, v194
	s_nop 1
	v_cndmask_b32_e64 v194, v194, v235, s[6:7]
	v_cmp_gt_f32_e64 s[8:9], v237, v194
	s_nop 1
	v_cndmask_b32_e64 v194, v194, v237, s[8:9]
	v_cmp_gt_f32_e64 s[10:11], v215, v194
	s_nop 1
	v_cndmask_b32_e64 v216, v194, v215, s[10:11]
	v_cndmask_b32_e64 v194, 0, 1, vcc
	v_cndmask_b32_e64 v194, v194, 2, s[0:1]
	v_cndmask_b32_e64 v194, v194, 3, s[4:5]
	v_cndmask_b32_e64 v194, v194, 4, s[6:7]
	v_cndmask_b32_e64 v194, v194, 5, s[8:9]
	v_cndmask_b32_e64 v194, v194, 6, s[10:11]
	v_cmp_ngt_f32_e32 vcc, v195, v216
	s_and_b64 s[16:17], s[10:11], vcc
	s_nop 0
	v_cndmask_b32_e32 v194, 7, v194, vcc
	v_cmp_eq_u32_e64 s[12:13], 0, v194
	s_or_b64 s[12:13], s[12:13], s[14:15]
	v_cmp_ne_u32_e64 s[10:11], 1, v194
	v_cndmask_b32_e64 v196, v196, v231, s[12:13]
	v_cmp_gt_f32_e64 s[14:15], v197, v196
	s_and_b64 s[10:11], s[10:11], s[14:15]
	v_cndmask_b32_e64 v196, v196, v197, s[10:11]
	v_cmp_ne_u32_e64 s[8:9], 2, v194
	v_cmp_gt_f32_e64 s[14:15], v214, v196
	s_and_b64 s[8:9], s[8:9], s[14:15]
	v_cndmask_b32_e64 v196, v196, v214, s[8:9]
	v_cmp_ne_u32_e64 s[6:7], 3, v194
	v_cmp_gt_f32_e64 s[14:15], v233, v196
	s_and_b64 s[6:7], s[6:7], s[14:15]
	v_cndmask_b32_e64 v196, v196, v233, s[6:7]
	v_cmp_ne_u32_e64 s[4:5], 4, v194
	v_cmp_gt_f32_e64 s[14:15], v235, v196
	s_and_b64 s[4:5], s[4:5], s[14:15]
	v_cndmask_b32_e64 v196, v196, v235, s[4:5]
	v_cmp_ne_u32_e64 s[0:1], 5, v194
	v_cmp_gt_f32_e64 s[14:15], v237, v196
	s_and_b64 s[0:1], s[0:1], s[14:15]
	v_cndmask_b32_e64 v196, v196, v237, s[0:1]
	v_cmp_ngt_f32_e64 s[14:15], v215, v196
	s_or_b64 s[14:15], s[16:17], s[14:15]
	v_cndmask_b32_e64 v197, 0, -1, s[12:13]
	v_cndmask_b32_e64 v196, v215, v196, s[14:15]
	v_cmp_gt_f32_e64 s[16:17], v195, v196
	s_and_b64 s[16:17], vcc, s[16:17]
	v_cndmask_b32_e64 v197, v197, 1, s[10:11]
	v_cndmask_b32_e64 v196, v196, v195, s[16:17]
	v_cndmask_b32_e32 v195, v195, v216, vcc
	v_sub_f32_e32 v195, v196, v195
	v_mul_f32_e32 v195, 0x3fb8aa3b, v195
	v_exp_f32_e32 v215, v195
	v_cndmask_b32_e64 v195, v197, 2, s[8:9]
	v_cndmask_b32_e64 v195, v195, 3, s[6:7]
	v_cndmask_b32_e64 v195, v195, 4, s[4:5]
	v_add_f32_e32 v214, 1.0, v215
	v_div_scale_f32 v196, s[4:5], v214, v214, 1.0
	v_rcp_f32_e32 v216, v196
	v_cndmask_b32_e64 v195, v195, 5, s[0:1]
	v_cndmask_b32_e64 v195, 6, v195, s[14:15]
	v_cndmask_b32_e64 v195, v195, 7, s[16:17]
	v_fma_f32 v197, -v196, v216, 1.0
	v_fmac_f32_e32 v216, v197, v216
	v_div_scale_f32 v197, vcc, 1.0, v214, 1.0
	v_mul_f32_e32 v217, v197, v216
	v_fma_f32 v218, -v196, v217, v197
	v_fmac_f32_e32 v217, v218, v216
	v_fma_f32 v218, -v196, v217, v197
	v_lshl_add_u32 v196, v194, 2, 0
	ds_add_rtn_u32 v196, v196, v230
	v_lshl_add_u32 v197, v195, 2, 0
	ds_add_rtn_u32 v197, v197, v230
	v_div_fmas_f32 v216, v218, v216, v217
	v_div_fixup_f32 v214, v216, v214, 1.0
	v_mul_f32_e32 v215, v215, v214
	s_waitcnt lgkmcnt(0)
	ds_write_b128 v226, v[194:197]
	v_lshl_add_u64 v[194:195], s[94:95], 0, v[206:207]
	v_add_co_u32_e32 v194, vcc, 0x280000, v194
	s_nop 1
	v_addc_co_u32_e32 v195, vcc, 0, v195, vcc
	global_store_dwordx2 v[194:195], v[214:215], off

	.amdhsa_kernel _Z10fwd_kernel4Args
		.amdhsa_group_segment_fixed_size 0
		.amdhsa_private_segment_fixed_size 0
		.amdhsa_kernarg_size 464
		.amdhsa_user_sgpr_count 2
		.amdhsa_user_sgpr_dispatch_ptr 0
		.amdhsa_user_sgpr_queue_ptr 0
		.amdhsa_user_sgpr_kernarg_segment_ptr 1
		.amdhsa_user_sgpr_dispatch_id 0
		.amdhsa_user_sgpr_kernarg_preload_length 0
		.amdhsa_user_sgpr_kernarg_preload_offset 0
		.amdhsa_user_sgpr_private_segment_size 0
		.amdhsa_uses_dynamic_stack 0
		.amdhsa_enable_private_segment 0
		.amdhsa_system_sgpr_workgroup_id_x 1
		.amdhsa_system_sgpr_workgroup_id_y 0
		.amdhsa_system_sgpr_workgroup_id_z 0
		.amdhsa_system_sgpr_workgroup_info 0
		.amdhsa_system_vgpr_workitem_id 0
		.amdhsa_next_free_vgpr 256
		.amdhsa_next_free_sgpr 102
		.amdhsa_accum_offset 256
		.amdhsa_reserve_vcc 1
		.amdhsa_float_round_mode_32 0
		.amdhsa_float_round_mode_16_64 0
		.amdhsa_float_denorm_mode_32 3
		.amdhsa_float_denorm_mode_16_64 3
		.amdhsa_dx10_clamp 1
		.amdhsa_ieee_mode 1
		.amdhsa_fp16_overflow 0
		.amdhsa_tg_split 0
		.amdhsa_exception_fp_ieee_invalid_op 0
		.amdhsa_exception_fp_denorm_src 0
		.amdhsa_exception_fp_ieee_div_zero 0
		.amdhsa_exception_fp_ieee_overflow 0
		.amdhsa_exception_fp_ieee_underflow 0
		.amdhsa_exception_fp_ieee_inexact 0
		.amdhsa_exception_int_div_zero 0
	.end_amdhsa_kernel

amdhsa.kernels:
  - .agpr_count:     0
    .args:
      - .offset:         0
        .size:           208
        .value_kind:     by_value
      - .offset:         208
        .size:           4
        .value_kind:     hidden_block_count_x
      - .offset:         212
        .size:           4
        .value_kind:     hidden_block_count_y
      - .offset:         216
        .size:           4
        .value_kind:     hidden_block_count_z
      - .offset:         220
        .size:           2
        .value_kind:     hidden_group_size_x
      - .offset:         222
        .size:           2
        .value_kind:     hidden_group_size_y
      - .offset:         224
        .size:           2
        .value_kind:     hidden_group_size_z
      - .offset:         226
        .size:           2
        .value_kind:     hidden_remainder_x
      - .offset:         228
        .size:           2
        .value_kind:     hidden_remainder_y
      - .offset:         230
        .size:           2
        .value_kind:     hidden_remainder_z
      - .offset:         248
        .size:           8
        .value_kind:     hidden_global_offset_x
      - .offset:         256
        .size:           8
        .value_kind:     hidden_global_offset_y
      - .offset:         264
        .size:           8
        .value_kind:     hidden_global_offset_z
      - .offset:         272
        .size:           2
        .value_kind:     hidden_grid_dims
      - .offset:         328
        .size:           4
        .value_kind:     hidden_dynamic_lds_size
    .group_segment_fixed_size: 0
    .kernarg_segment_align: 8
    .kernarg_segment_size: 464
    .language:       OpenCL C
    .language_version:
      - 2
      - 0
    .max_flat_workgroup_size: 512
    .name:           _Z10fwd_kernel4Args
    .private_segment_fixed_size: 0
    .sgpr_count:     108
    .sgpr_spill_count: 118
    .symbol:         _Z10fwd_kernel4Args.kd
    .uniform_work_group_size: 1
    .uses_dynamic_stack: false
    .vgpr_count:     256
    .vgpr_spill_count: 0
    .wavefront_size: 64
